# speedup vs baseline: 1.2521x; 1.0020x over previous
.LBB0_65:
	s_or_b64 exec, exec, s[12:13]
	v_mov_b32_e32 v0, 0x20000
	s_waitcnt lgkmcnt(0)
	s_barrier
	ds_read_b96 v[186:188], v0
	v_lshlrev_b32_e32 v0, 10, v193
	s_load_dwordx4 s[12:15], s[0:1], 0x8
	v_and_b32_e32 v0, 0xc00, v0
	v_lshlrev_b32_e32 v1, 1, v193
	s_waitcnt lgkmcnt(0)
	v_readfirstlane_b32 s18, v188
	s_lshl_b32 s2, s18, 5
	v_add_u32_e32 v0, s2, v0
	v_bfe_u32 v109, v193, 4, 2
	v_and_or_b32 v0, v1, 24, v0
	s_lshr_b32 s3, s3, 6
	v_lshlrev_b32_e32 v217, 3, v109
	v_ashrrev_i32_e32 v1, 31, v0
	v_lshl_or_b32 v200, s3, 8, v217
	v_lshlrev_b64 v[4:5], 2, v[0:1]
	v_mov_b32_e32 v201, 0
	v_lshl_add_u64 v[6:7], s[14:15], 0, v[4:5]
	v_lshlrev_b64 v[0:1], 14, v[200:201]
	v_lshl_add_u64 v[0:1], v[6:7], 0, v[0:1]
	global_load_dwordx4 v[8:11], v[0:1], off offset:16
	global_load_dwordx4 v[12:15], v[0:1], off
	v_or_b32_e32 v0, 1, v200
	v_mov_b32_e32 v1, v201
	v_lshlrev_b64 v[0:1], 14, v[0:1]
	v_lshl_add_u64 v[0:1], v[6:7], 0, v[0:1]
	global_load_dwordx4 v[16:19], v[0:1], off offset:16
	global_load_dwordx4 v[20:23], v[0:1], off
	v_or_b32_e32 v0, 2, v200
	v_mov_b32_e32 v1, v201
	v_lshlrev_b64 v[0:1], 14, v[0:1]
	v_lshl_add_u64 v[0:1], v[6:7], 0, v[0:1]
	global_load_dwordx4 v[24:27], v[0:1], off offset:16
	global_load_dwordx4 v[28:31], v[0:1], off
	v_or_b32_e32 v0, 3, v200
	v_mov_b32_e32 v1, v201
	v_lshlrev_b64 v[0:1], 14, v[0:1]
	v_lshl_add_u64 v[0:1], v[6:7], 0, v[0:1]
	global_load_dwordx4 v[32:35], v[0:1], off offset:16
	global_load_dwordx4 v[36:39], v[0:1], off
	v_or_b32_e32 v0, 4, v200
	v_mov_b32_e32 v1, v201
	v_lshlrev_b64 v[0:1], 14, v[0:1]
	v_lshl_add_u64 v[0:1], v[6:7], 0, v[0:1]
	global_load_dwordx4 v[40:43], v[0:1], off offset:16
	global_load_dwordx4 v[44:47], v[0:1], off
	v_or_b32_e32 v0, 5, v200
	v_mov_b32_e32 v1, v201
	v_lshlrev_b64 v[0:1], 14, v[0:1]
	v_lshl_add_u64 v[0:1], v[6:7], 0, v[0:1]
	global_load_dwordx4 v[48:51], v[0:1], off offset:16
	global_load_dwordx4 v[52:55], v[0:1], off
	v_or_b32_e32 v0, 6, v200
	v_mov_b32_e32 v1, v201
	v_lshlrev_b64 v[0:1], 14, v[0:1]
	v_lshl_add_u64 v[0:1], v[6:7], 0, v[0:1]
	global_load_dwordx4 v[56:59], v[0:1], off offset:16
	global_load_dwordx4 v[60:63], v[0:1], off
	v_or_b32_e32 v0, 7, v200
	v_mov_b32_e32 v1, v201
	v_lshlrev_b64 v[0:1], 14, v[0:1]
	v_lshl_add_u64 v[0:1], v[6:7], 0, v[0:1]
	global_load_dwordx4 v[64:67], v[0:1], off offset:16
	global_load_dwordx4 v[68:71], v[0:1], off
	v_mov_b32_e32 v1, v201
	s_lshl_b32 s14, s3, 7
	v_and_b32_e32 v198, 63, v193
	v_lshlrev_b32_e32 v108, 4, v198
	v_lshl_or_b32 v95, s3, 15, v108
	s_lshl_b32 s0, s3, 11
	v_bfe_u32 v207, v193, 3, 3
	s_lshl_b32 s20, s3, 3
	v_or_b32_e32 v208, s20, v207
	v_readfirstlane_b32 s19, v187
	v_and_b32_e32 v150, 7, v193
	s_mov_b32 s15, 0
	v_or_b32_e32 v198, s0, v198
	s_mov_b32 s24, s15
	s_mov_b32 s25, s15
	s_mov_b32 s26, s15
	s_mov_b32 s27, s15
	v_and_b32_e32 v220, 15, v193
	s_lshl_b32 s22, s18, 2
	s_add_i32 s22, s22, s3
	s_lshl_b32 s21, s3, 12
	s_and_b32 s3, s22, 7
	s_ashr_i32 s23, s22, 3
	s_and_b32 s9, s9, 0xffff
	s_add_i32 s23, s23, 16
	v_mov_b32_e32 v202, v201
	v_mov_b32_e32 v203, v201
	s_mov_b32 s11, 0x20000
	s_mov_b32 s10, 0x40000
	s_waitcnt vmcnt(12)
	v_cvt_pk_f16_f32 v231, v12, v20
	v_accvgpr_write_b32 a0, v231
	s_waitcnt vmcnt(8)
	v_cvt_pk_f16_f32 v230, v28, v36
	v_accvgpr_write_b32 a1, v230
	s_waitcnt vmcnt(4)
	v_cvt_pk_f16_f32 v229, v44, v52
	v_accvgpr_write_b32 a2, v229
	s_waitcnt vmcnt(1)
	v_cvt_pk_f16_f32 v0, v56, v64
	v_accvgpr_write_b32 a131, v0
	v_cvt_pk_f16_f32 v0, v40, v48
	v_accvgpr_write_b32 a130, v0
	v_cvt_pk_f16_f32 v0, v24, v32
	v_accvgpr_write_b32 a129, v0
	v_cvt_pk_f16_f32 v0, v8, v16
	v_accvgpr_write_b32 a128, v0
	s_waitcnt vmcnt(0)
	v_cvt_pk_f16_f32 v0, v61, v69
	v_accvgpr_write_b32 a35, v0
	v_cvt_pk_f16_f32 v0, v45, v53
	v_accvgpr_write_b32 a34, v0
	v_cvt_pk_f16_f32 v0, v29, v37
	v_accvgpr_write_b32 a33, v0
	v_cvt_pk_f16_f32 v0, v13, v21
	v_accvgpr_write_b32 a32, v0
	v_cvt_pk_f16_f32 v0, v57, v65
	v_accvgpr_write_b32 a163, v0
	v_cvt_pk_f16_f32 v0, v41, v49
	v_accvgpr_write_b32 a162, v0
	v_cvt_pk_f16_f32 v0, v25, v33
	v_accvgpr_write_b32 a161, v0
	v_cvt_pk_f16_f32 v0, v9, v17
	v_accvgpr_write_b32 a160, v0
	v_cvt_pk_f16_f32 v0, v62, v70
	v_accvgpr_write_b32 a67, v0
	v_cvt_pk_f16_f32 v0, v46, v54
	v_accvgpr_write_b32 a66, v0
	v_cvt_pk_f16_f32 v0, v30, v38
	v_accvgpr_write_b32 a65, v0
	v_cvt_pk_f16_f32 v0, v14, v22
	v_accvgpr_write_b32 a64, v0
	v_cvt_pk_f16_f32 v0, v58, v66
	v_accvgpr_write_b32 a195, v0
	v_cvt_pk_f16_f32 v0, v42, v50
	v_accvgpr_write_b32 a194, v0
	v_cvt_pk_f16_f32 v0, v26, v34
	v_accvgpr_write_b32 a193, v0
	v_cvt_pk_f16_f32 v0, v10, v18
	v_accvgpr_write_b32 a192, v0
	v_cvt_pk_f16_f32 v0, v63, v71
	v_accvgpr_write_b32 a99, v0
	v_cvt_pk_f16_f32 v0, v47, v55
	v_accvgpr_write_b32 a98, v0
	v_cvt_pk_f16_f32 v0, v31, v39
	v_accvgpr_write_b32 a97, v0
	v_cvt_pk_f16_f32 v0, v15, v23
	v_accvgpr_write_b32 a96, v0
	v_cvt_pk_f16_f32 v0, v59, v67
	v_accvgpr_write_b32 a227, v0
	v_cvt_pk_f16_f32 v0, v43, v51
	v_accvgpr_write_b32 a226, v0
	v_cvt_pk_f16_f32 v0, v27, v35
	v_accvgpr_write_b32 a225, v0
	v_cvt_pk_f16_f32 v0, v11, v19
	v_accvgpr_write_b32 a224, v0
	v_or_b32_e32 v0, 32, v200
	v_lshlrev_b64 v[0:1], 14, v[0:1]
	v_lshl_add_u64 v[0:1], v[6:7], 0, v[0:1]
	global_load_dwordx4 v[8:11], v[0:1], off offset:16
	global_load_dwordx4 v[12:15], v[0:1], off
	v_or_b32_e32 v0, 33, v200
	v_mov_b32_e32 v1, v201
	v_lshlrev_b64 v[0:1], 14, v[0:1]
	v_lshl_add_u64 v[0:1], v[6:7], 0, v[0:1]
	global_load_dwordx4 v[16:19], v[0:1], off offset:16
	global_load_dwordx4 v[20:23], v[0:1], off
	v_or_b32_e32 v0, 34, v200
	v_mov_b32_e32 v1, v201
	v_lshlrev_b64 v[0:1], 14, v[0:1]
	v_lshl_add_u64 v[0:1], v[6:7], 0, v[0:1]
	global_load_dwordx4 v[24:27], v[0:1], off offset:16
	global_load_dwordx4 v[28:31], v[0:1], off
	v_or_b32_e32 v0, 35, v200
	v_mov_b32_e32 v1, v201
	v_lshlrev_b64 v[0:1], 14, v[0:1]
	v_lshl_add_u64 v[0:1], v[6:7], 0, v[0:1]
	global_load_dwordx4 v[32:35], v[0:1], off offset:16
	global_load_dwordx4 v[36:39], v[0:1], off
	v_or_b32_e32 v0, 36, v200
	v_mov_b32_e32 v1, v201
	v_lshlrev_b64 v[0:1], 14, v[0:1]
	v_lshl_add_u64 v[0:1], v[6:7], 0, v[0:1]
	global_load_dwordx4 v[40:43], v[0:1], off offset:16
	global_load_dwordx4 v[44:47], v[0:1], off
	v_or_b32_e32 v0, 37, v200
	v_mov_b32_e32 v1, v201
	v_lshlrev_b64 v[0:1], 14, v[0:1]
	v_lshl_add_u64 v[0:1], v[6:7], 0, v[0:1]
	global_load_dwordx4 v[48:51], v[0:1], off offset:16
	global_load_dwordx4 v[52:55], v[0:1], off
	v_or_b32_e32 v0, 38, v200
	v_mov_b32_e32 v1, v201
	v_lshlrev_b64 v[0:1], 14, v[0:1]
	v_lshl_add_u64 v[0:1], v[6:7], 0, v[0:1]
	v_cvt_pk_f16_f32 v228, v60, v68
	global_load_dwordx4 v[56:59], v[0:1], off offset:16
	global_load_dwordx4 v[60:63], v[0:1], off
	v_or_b32_e32 v0, 39, v200
	v_mov_b32_e32 v1, v201
	v_lshlrev_b64 v[0:1], 14, v[0:1]
	v_lshl_add_u64 v[0:1], v[6:7], 0, v[0:1]
	global_load_dwordx4 v[64:67], v[0:1], off offset:16
	global_load_dwordx4 v[68:71], v[0:1], off
	v_mov_b32_e32 v1, v201
	v_accvgpr_write_b32 a3, v228
	s_waitcnt vmcnt(12)
	v_cvt_pk_f16_f32 v206, v12, v20
	v_accvgpr_write_b32 a4, v206
	s_waitcnt vmcnt(8)
	v_cvt_pk_f16_f32 v197, v28, v36
	v_accvgpr_write_b32 a5, v197
	s_waitcnt vmcnt(4)
	v_cvt_pk_f16_f32 v199, v44, v52
	v_accvgpr_write_b32 a6, v199
	s_waitcnt vmcnt(1)
	v_cvt_pk_f16_f32 v0, v56, v64
	v_accvgpr_write_b32 a135, v0
	v_cvt_pk_f16_f32 v0, v40, v48
	v_accvgpr_write_b32 a134, v0
	v_cvt_pk_f16_f32 v0, v24, v32
	v_accvgpr_write_b32 a133, v0
	v_cvt_pk_f16_f32 v0, v8, v16
	v_accvgpr_write_b32 a132, v0
	s_waitcnt vmcnt(0)
	v_cvt_pk_f16_f32 v0, v61, v69
	v_accvgpr_write_b32 a39, v0
	v_cvt_pk_f16_f32 v0, v45, v53
	v_accvgpr_write_b32 a38, v0
	v_cvt_pk_f16_f32 v0, v29, v37
	v_accvgpr_write_b32 a37, v0
	v_cvt_pk_f16_f32 v0, v13, v21
	v_accvgpr_write_b32 a36, v0
	v_cvt_pk_f16_f32 v0, v57, v65
	v_accvgpr_write_b32 a167, v0
	v_cvt_pk_f16_f32 v0, v41, v49
	v_accvgpr_write_b32 a166, v0
	v_cvt_pk_f16_f32 v0, v25, v33
	v_accvgpr_write_b32 a165, v0
	v_cvt_pk_f16_f32 v0, v9, v17
	v_accvgpr_write_b32 a164, v0
	v_cvt_pk_f16_f32 v0, v62, v70
	v_accvgpr_write_b32 a71, v0
	v_cvt_pk_f16_f32 v0, v46, v54
	v_accvgpr_write_b32 a70, v0
	v_cvt_pk_f16_f32 v0, v30, v38
	v_accvgpr_write_b32 a69, v0
	v_cvt_pk_f16_f32 v0, v14, v22
	v_accvgpr_write_b32 a68, v0
	v_cvt_pk_f16_f32 v0, v58, v66
	v_accvgpr_write_b32 a199, v0
	v_cvt_pk_f16_f32 v0, v42, v50
	v_accvgpr_write_b32 a198, v0
	v_cvt_pk_f16_f32 v0, v26, v34
	v_accvgpr_write_b32 a197, v0
	v_cvt_pk_f16_f32 v0, v10, v18
	v_accvgpr_write_b32 a196, v0
	v_cvt_pk_f16_f32 v0, v63, v71
	v_accvgpr_write_b32 a103, v0
	v_cvt_pk_f16_f32 v0, v47, v55
	v_accvgpr_write_b32 a102, v0
	v_cvt_pk_f16_f32 v0, v31, v39
	v_accvgpr_write_b32 a101, v0
	v_cvt_pk_f16_f32 v0, v15, v23
	v_accvgpr_write_b32 a100, v0
	v_cvt_pk_f16_f32 v0, v59, v67
	v_accvgpr_write_b32 a231, v0
	v_cvt_pk_f16_f32 v0, v43, v51
	v_accvgpr_write_b32 a230, v0
	v_cvt_pk_f16_f32 v0, v27, v35
	v_accvgpr_write_b32 a229, v0
	v_cvt_pk_f16_f32 v0, v11, v19
	v_accvgpr_write_b32 a228, v0
	v_or_b32_e32 v0, 64, v200
	v_lshlrev_b64 v[0:1], 14, v[0:1]
	v_lshl_add_u64 v[0:1], v[6:7], 0, v[0:1]
	global_load_dwordx4 v[8:11], v[0:1], off offset:16
	global_load_dwordx4 v[12:15], v[0:1], off
	v_or_b32_e32 v0, 0x41, v200
	v_mov_b32_e32 v1, v201
	v_lshlrev_b64 v[0:1], 14, v[0:1]
	v_lshl_add_u64 v[0:1], v[6:7], 0, v[0:1]
	global_load_dwordx4 v[16:19], v[0:1], off offset:16
	global_load_dwordx4 v[20:23], v[0:1], off
	v_or_b32_e32 v0, 0x42, v200
	v_mov_b32_e32 v1, v201
	v_lshlrev_b64 v[0:1], 14, v[0:1]
	v_lshl_add_u64 v[0:1], v[6:7], 0, v[0:1]
	global_load_dwordx4 v[24:27], v[0:1], off offset:16
	global_load_dwordx4 v[28:31], v[0:1], off
	v_or_b32_e32 v0, 0x43, v200
	v_mov_b32_e32 v1, v201
	v_lshlrev_b64 v[0:1], 14, v[0:1]
	v_lshl_add_u64 v[0:1], v[6:7], 0, v[0:1]
	global_load_dwordx4 v[32:35], v[0:1], off offset:16
	global_load_dwordx4 v[36:39], v[0:1], off
	v_or_b32_e32 v0, 0x44, v200
	v_mov_b32_e32 v1, v201
	v_lshlrev_b64 v[0:1], 14, v[0:1]
	v_lshl_add_u64 v[0:1], v[6:7], 0, v[0:1]
	global_load_dwordx4 v[40:43], v[0:1], off offset:16
	global_load_dwordx4 v[44:47], v[0:1], off
	v_or_b32_e32 v0, 0x45, v200
	v_mov_b32_e32 v1, v201
	v_lshlrev_b64 v[0:1], 14, v[0:1]
	v_lshl_add_u64 v[0:1], v[6:7], 0, v[0:1]
	global_load_dwordx4 v[48:51], v[0:1], off offset:16
	global_load_dwordx4 v[52:55], v[0:1], off
	v_or_b32_e32 v0, 0x46, v200
	v_mov_b32_e32 v1, v201
	v_lshlrev_b64 v[0:1], 14, v[0:1]
	v_lshl_add_u64 v[0:1], v[6:7], 0, v[0:1]
	v_cvt_pk_f16_f32 v205, v60, v68
	global_load_dwordx4 v[56:59], v[0:1], off offset:16
	global_load_dwordx4 v[60:63], v[0:1], off
	v_or_b32_e32 v0, 0x47, v200
	v_mov_b32_e32 v1, v201
	v_lshlrev_b64 v[0:1], 14, v[0:1]
	v_lshl_add_u64 v[0:1], v[6:7], 0, v[0:1]
	global_load_dwordx4 v[64:67], v[0:1], off offset:16
	global_load_dwordx4 v[68:71], v[0:1], off
	v_mov_b32_e32 v1, v201
	v_accvgpr_write_b32 a7, v205
	s_waitcnt vmcnt(12)
	v_cvt_pk_f16_f32 v155, v12, v20
	v_accvgpr_write_b32 a8, v155
	s_waitcnt vmcnt(8)
	v_cvt_pk_f16_f32 v156, v28, v36
	v_accvgpr_write_b32 a9, v156
	s_waitcnt vmcnt(4)
	v_cvt_pk_f16_f32 v157, v44, v52
	v_accvgpr_write_b32 a10, v157
	s_waitcnt vmcnt(1)
	v_cvt_pk_f16_f32 v0, v56, v64
	v_accvgpr_write_b32 a139, v0
	v_cvt_pk_f16_f32 v0, v40, v48
	v_accvgpr_write_b32 a138, v0
	v_cvt_pk_f16_f32 v0, v24, v32
	v_accvgpr_write_b32 a137, v0
	v_cvt_pk_f16_f32 v0, v8, v16
	v_accvgpr_write_b32 a136, v0
	s_waitcnt vmcnt(0)
	v_cvt_pk_f16_f32 v0, v61, v69
	v_accvgpr_write_b32 a43, v0
	v_cvt_pk_f16_f32 v0, v45, v53
	v_accvgpr_write_b32 a42, v0
	v_cvt_pk_f16_f32 v0, v29, v37
	v_accvgpr_write_b32 a41, v0
	v_cvt_pk_f16_f32 v0, v13, v21
	v_accvgpr_write_b32 a40, v0
	v_cvt_pk_f16_f32 v0, v57, v65
	v_accvgpr_write_b32 a171, v0
	v_cvt_pk_f16_f32 v0, v41, v49
	v_accvgpr_write_b32 a170, v0
	v_cvt_pk_f16_f32 v0, v25, v33
	v_accvgpr_write_b32 a169, v0
	v_cvt_pk_f16_f32 v0, v9, v17
	v_accvgpr_write_b32 a168, v0
	v_cvt_pk_f16_f32 v0, v62, v70
	v_accvgpr_write_b32 a75, v0
	v_cvt_pk_f16_f32 v0, v46, v54
	v_accvgpr_write_b32 a74, v0
	v_cvt_pk_f16_f32 v0, v30, v38
	v_accvgpr_write_b32 a73, v0
	v_cvt_pk_f16_f32 v0, v14, v22
	v_accvgpr_write_b32 a72, v0
	v_cvt_pk_f16_f32 v0, v58, v66
	v_accvgpr_write_b32 a203, v0
	v_cvt_pk_f16_f32 v0, v42, v50
	v_accvgpr_write_b32 a202, v0
	v_cvt_pk_f16_f32 v0, v26, v34
	v_accvgpr_write_b32 a201, v0
	v_cvt_pk_f16_f32 v0, v10, v18
	v_accvgpr_write_b32 a200, v0
	v_cvt_pk_f16_f32 v0, v63, v71
	v_accvgpr_write_b32 a107, v0
	v_cvt_pk_f16_f32 v0, v47, v55
	v_accvgpr_write_b32 a106, v0
	v_cvt_pk_f16_f32 v0, v31, v39
	v_accvgpr_write_b32 a105, v0
	v_cvt_pk_f16_f32 v0, v15, v23
	v_accvgpr_write_b32 a104, v0
	v_cvt_pk_f16_f32 v0, v59, v67
	v_accvgpr_write_b32 a235, v0
	v_cvt_pk_f16_f32 v0, v43, v51
	v_accvgpr_write_b32 a234, v0
	v_cvt_pk_f16_f32 v0, v27, v35
	v_accvgpr_write_b32 a233, v0
	v_cvt_pk_f16_f32 v0, v11, v19
	v_accvgpr_write_b32 a232, v0
	v_or_b32_e32 v0, 0x60, v200
	v_lshlrev_b64 v[0:1], 14, v[0:1]
	v_lshl_add_u64 v[0:1], v[6:7], 0, v[0:1]
	global_load_dwordx4 v[8:11], v[0:1], off offset:16
	global_load_dwordx4 v[12:15], v[0:1], off
	v_or_b32_e32 v0, 0x61, v200
	v_mov_b32_e32 v1, v201
	v_lshlrev_b64 v[0:1], 14, v[0:1]
	v_lshl_add_u64 v[0:1], v[6:7], 0, v[0:1]
	global_load_dwordx4 v[16:19], v[0:1], off offset:16
	global_load_dwordx4 v[20:23], v[0:1], off
	v_or_b32_e32 v0, 0x62, v200
	v_mov_b32_e32 v1, v201
	v_lshlrev_b64 v[0:1], 14, v[0:1]
	v_lshl_add_u64 v[0:1], v[6:7], 0, v[0:1]
	global_load_dwordx4 v[24:27], v[0:1], off offset:16
	global_load_dwordx4 v[28:31], v[0:1], off
	v_or_b32_e32 v0, 0x63, v200
	v_mov_b32_e32 v1, v201
	v_lshlrev_b64 v[0:1], 14, v[0:1]
	v_lshl_add_u64 v[0:1], v[6:7], 0, v[0:1]
	global_load_dwordx4 v[32:35], v[0:1], off offset:16
	global_load_dwordx4 v[36:39], v[0:1], off
	v_or_b32_e32 v0, 0x64, v200
	v_mov_b32_e32 v1, v201
	v_lshlrev_b64 v[0:1], 14, v[0:1]
	v_lshl_add_u64 v[0:1], v[6:7], 0, v[0:1]
	global_load_dwordx4 v[40:43], v[0:1], off offset:16
	global_load_dwordx4 v[44:47], v[0:1], off
	v_or_b32_e32 v0, 0x65, v200
	v_mov_b32_e32 v1, v201
	v_lshlrev_b64 v[0:1], 14, v[0:1]
	v_lshl_add_u64 v[0:1], v[6:7], 0, v[0:1]
	global_load_dwordx4 v[48:51], v[0:1], off offset:16
	global_load_dwordx4 v[52:55], v[0:1], off
	v_or_b32_e32 v0, 0x66, v200
	v_mov_b32_e32 v1, v201
	v_lshlrev_b64 v[0:1], 14, v[0:1]
	v_lshl_add_u64 v[0:1], v[6:7], 0, v[0:1]
	v_cvt_pk_f16_f32 v158, v60, v68
	global_load_dwordx4 v[56:59], v[0:1], off offset:16
	global_load_dwordx4 v[60:63], v[0:1], off
	v_or_b32_e32 v0, 0x67, v200
	v_mov_b32_e32 v1, v201
	v_lshlrev_b64 v[0:1], 14, v[0:1]
	v_lshl_add_u64 v[0:1], v[6:7], 0, v[0:1]
	global_load_dwordx4 v[64:67], v[0:1], off offset:16
	global_load_dwordx4 v[68:71], v[0:1], off
	v_mov_b32_e32 v1, v201
	v_accvgpr_write_b32 a11, v158
	s_waitcnt vmcnt(12)
	v_cvt_pk_f16_f32 v122, v12, v20
	v_accvgpr_write_b32 a12, v122
	s_waitcnt vmcnt(8)
	v_cvt_pk_f16_f32 v123, v28, v36
	v_accvgpr_write_b32 a13, v123
	s_waitcnt vmcnt(4)
	v_cvt_pk_f16_f32 v124, v44, v52
	v_accvgpr_write_b32 a14, v124
	s_waitcnt vmcnt(1)
	v_cvt_pk_f16_f32 v0, v56, v64
	v_accvgpr_write_b32 a143, v0
	v_cvt_pk_f16_f32 v0, v40, v48
	v_accvgpr_write_b32 a142, v0
	v_cvt_pk_f16_f32 v0, v24, v32
	v_accvgpr_write_b32 a141, v0
	v_cvt_pk_f16_f32 v0, v8, v16
	v_accvgpr_write_b32 a140, v0
	s_waitcnt vmcnt(0)
	v_cvt_pk_f16_f32 v0, v61, v69
	v_accvgpr_write_b32 a47, v0
	v_cvt_pk_f16_f32 v0, v45, v53
	v_accvgpr_write_b32 a46, v0
	v_cvt_pk_f16_f32 v0, v29, v37
	v_accvgpr_write_b32 a45, v0
	v_cvt_pk_f16_f32 v0, v13, v21
	v_accvgpr_write_b32 a44, v0
	v_cvt_pk_f16_f32 v0, v57, v65
	v_accvgpr_write_b32 a175, v0
	v_cvt_pk_f16_f32 v0, v41, v49
	v_accvgpr_write_b32 a174, v0
	v_cvt_pk_f16_f32 v0, v25, v33
	v_accvgpr_write_b32 a173, v0
	v_cvt_pk_f16_f32 v0, v9, v17
	v_accvgpr_write_b32 a172, v0
	v_cvt_pk_f16_f32 v0, v62, v70
	v_accvgpr_write_b32 a79, v0
	v_cvt_pk_f16_f32 v0, v46, v54
	v_accvgpr_write_b32 a78, v0
	v_cvt_pk_f16_f32 v0, v30, v38
	v_accvgpr_write_b32 a77, v0
	v_cvt_pk_f16_f32 v0, v14, v22
	v_accvgpr_write_b32 a76, v0
	v_cvt_pk_f16_f32 v0, v58, v66
	v_accvgpr_write_b32 a207, v0
	v_cvt_pk_f16_f32 v0, v42, v50
	v_accvgpr_write_b32 a206, v0
	v_cvt_pk_f16_f32 v0, v26, v34
	v_accvgpr_write_b32 a205, v0
	v_cvt_pk_f16_f32 v0, v10, v18
	v_accvgpr_write_b32 a204, v0
	v_cvt_pk_f16_f32 v0, v63, v71
	v_accvgpr_write_b32 a111, v0
	v_cvt_pk_f16_f32 v0, v47, v55
	v_accvgpr_write_b32 a110, v0
	v_cvt_pk_f16_f32 v0, v31, v39
	v_accvgpr_write_b32 a109, v0
	v_cvt_pk_f16_f32 v0, v15, v23
	v_accvgpr_write_b32 a108, v0
	v_cvt_pk_f16_f32 v0, v59, v67
	v_accvgpr_write_b32 a239, v0
	v_cvt_pk_f16_f32 v0, v43, v51
	v_accvgpr_write_b32 a238, v0
	v_cvt_pk_f16_f32 v0, v27, v35
	v_accvgpr_write_b32 a237, v0
	v_cvt_pk_f16_f32 v0, v11, v19
	v_accvgpr_write_b32 a236, v0
	v_or_b32_e32 v0, 0x80, v200
	v_lshlrev_b64 v[0:1], 14, v[0:1]
	v_lshl_add_u64 v[0:1], v[6:7], 0, v[0:1]
	global_load_dwordx4 v[8:11], v[0:1], off offset:16
	global_load_dwordx4 v[12:15], v[0:1], off
	v_or_b32_e32 v0, 0x81, v200
	v_mov_b32_e32 v1, v201
	v_lshlrev_b64 v[0:1], 14, v[0:1]
	v_lshl_add_u64 v[0:1], v[6:7], 0, v[0:1]
	global_load_dwordx4 v[16:19], v[0:1], off offset:16
	global_load_dwordx4 v[20:23], v[0:1], off
	v_or_b32_e32 v0, 0x82, v200
	v_mov_b32_e32 v1, v201
	v_lshlrev_b64 v[0:1], 14, v[0:1]
	v_lshl_add_u64 v[0:1], v[6:7], 0, v[0:1]
	global_load_dwordx4 v[24:27], v[0:1], off offset:16
	global_load_dwordx4 v[28:31], v[0:1], off
	v_or_b32_e32 v0, 0x83, v200
	v_mov_b32_e32 v1, v201
	v_lshlrev_b64 v[0:1], 14, v[0:1]
	v_lshl_add_u64 v[0:1], v[6:7], 0, v[0:1]
	global_load_dwordx4 v[32:35], v[0:1], off offset:16
	global_load_dwordx4 v[36:39], v[0:1], off
	v_or_b32_e32 v0, 0x84, v200
	v_mov_b32_e32 v1, v201
	v_lshlrev_b64 v[0:1], 14, v[0:1]
	v_lshl_add_u64 v[0:1], v[6:7], 0, v[0:1]
	global_load_dwordx4 v[40:43], v[0:1], off offset:16
	global_load_dwordx4 v[44:47], v[0:1], off
	v_or_b32_e32 v0, 0x85, v200
	v_mov_b32_e32 v1, v201
	v_lshlrev_b64 v[0:1], 14, v[0:1]
	v_lshl_add_u64 v[0:1], v[6:7], 0, v[0:1]
	global_load_dwordx4 v[48:51], v[0:1], off offset:16
	global_load_dwordx4 v[52:55], v[0:1], off
	v_or_b32_e32 v0, 0x86, v200
	v_mov_b32_e32 v1, v201
	v_lshlrev_b64 v[0:1], 14, v[0:1]
	v_lshl_add_u64 v[0:1], v[6:7], 0, v[0:1]
	v_cvt_pk_f16_f32 v125, v60, v68
	global_load_dwordx4 v[56:59], v[0:1], off offset:16
	global_load_dwordx4 v[60:63], v[0:1], off
	v_or_b32_e32 v0, 0x87, v200
	v_mov_b32_e32 v1, v201
	v_lshlrev_b64 v[0:1], 14, v[0:1]
	v_lshl_add_u64 v[0:1], v[6:7], 0, v[0:1]
	global_load_dwordx4 v[64:67], v[0:1], off offset:16
	global_load_dwordx4 v[68:71], v[0:1], off
	v_mov_b32_e32 v1, v201
	v_accvgpr_write_b32 a15, v125
	s_waitcnt vmcnt(12)
	v_cvt_pk_f16_f32 v114, v12, v20
	v_cvt_pk_f16_f32 v245, v13, v21
	v_cvt_pk_f16_f32 v235, v14, v22
	v_cvt_pk_f16_f32 v227, v15, v23
	v_accvgpr_write_b32 a16, v114
	v_accvgpr_write_b32 a48, v245
	v_accvgpr_write_b32 a80, v235
	v_accvgpr_write_b32 a112, v227
	s_waitcnt vmcnt(8)
	v_cvt_pk_f16_f32 v115, v28, v36
	v_cvt_pk_f16_f32 v243, v29, v37
	v_cvt_pk_f16_f32 v234, v30, v38
	v_cvt_pk_f16_f32 v226, v31, v39
	v_accvgpr_write_b32 a17, v115
	v_accvgpr_write_b32 a49, v243
	v_accvgpr_write_b32 a81, v234
	v_accvgpr_write_b32 a113, v226
	s_waitcnt vmcnt(4)
	v_cvt_pk_f16_f32 v116, v44, v52
	v_cvt_pk_f16_f32 v241, v45, v53
	v_cvt_pk_f16_f32 v233, v46, v54
	v_cvt_pk_f16_f32 v225, v47, v55
	v_accvgpr_write_b32 a18, v116
	v_accvgpr_write_b32 a50, v241
	v_accvgpr_write_b32 a82, v233
	v_accvgpr_write_b32 a114, v225
	s_waitcnt vmcnt(1)
	v_cvt_pk_f16_f32 v0, v56, v64
	v_accvgpr_write_b32 a147, v0
	v_cvt_pk_f16_f32 v0, v40, v48
	v_accvgpr_write_b32 a146, v0
	v_cvt_pk_f16_f32 v0, v24, v32
	v_accvgpr_write_b32 a145, v0
	v_cvt_pk_f16_f32 v0, v8, v16
	v_accvgpr_write_b32 a144, v0
	v_cvt_pk_f16_f32 v0, v57, v65
	v_accvgpr_write_b32 a179, v0
	v_cvt_pk_f16_f32 v0, v41, v49
	v_accvgpr_write_b32 a178, v0
	v_cvt_pk_f16_f32 v0, v25, v33
	v_accvgpr_write_b32 a177, v0
	v_cvt_pk_f16_f32 v0, v9, v17
	v_accvgpr_write_b32 a176, v0
	v_cvt_pk_f16_f32 v0, v58, v66
	v_accvgpr_write_b32 a211, v0
	v_cvt_pk_f16_f32 v0, v42, v50
	v_accvgpr_write_b32 a210, v0
	v_cvt_pk_f16_f32 v0, v26, v34
	v_accvgpr_write_b32 a209, v0
	v_cvt_pk_f16_f32 v0, v10, v18
	v_accvgpr_write_b32 a208, v0
	s_waitcnt vmcnt(0)
	v_cvt_pk_f16_f32 v0, v63, v71
	v_accvgpr_write_b32 a115, v0
	v_cvt_pk_f16_f32 v0, v59, v67
	v_accvgpr_write_b32 a243, v0
	v_cvt_pk_f16_f32 v0, v43, v51
	v_accvgpr_write_b32 a242, v0
	v_cvt_pk_f16_f32 v0, v27, v35
	v_accvgpr_write_b32 a241, v0
	v_cvt_pk_f16_f32 v0, v11, v19
	v_accvgpr_write_b32 a240, v0
	v_or_b32_e32 v0, 0xa0, v200
	v_lshlrev_b64 v[0:1], 14, v[0:1]
	v_lshl_add_u64 v[0:1], v[6:7], 0, v[0:1]
	global_load_dwordx4 v[8:11], v[0:1], off offset:16
	global_load_dwordx4 v[12:15], v[0:1], off
	v_or_b32_e32 v0, 0xa1, v200
	v_mov_b32_e32 v1, v201
	v_lshlrev_b64 v[0:1], 14, v[0:1]
	v_lshl_add_u64 v[0:1], v[6:7], 0, v[0:1]
	global_load_dwordx4 v[16:19], v[0:1], off offset:16
	global_load_dwordx4 v[20:23], v[0:1], off
	v_or_b32_e32 v0, 0xa2, v200
	v_mov_b32_e32 v1, v201
	v_lshlrev_b64 v[0:1], 14, v[0:1]
	v_lshl_add_u64 v[0:1], v[6:7], 0, v[0:1]
	global_load_dwordx4 v[24:27], v[0:1], off offset:16
	global_load_dwordx4 v[28:31], v[0:1], off
	v_or_b32_e32 v0, 0xa3, v200
	v_mov_b32_e32 v1, v201
	v_lshlrev_b64 v[0:1], 14, v[0:1]
	v_lshl_add_u64 v[0:1], v[6:7], 0, v[0:1]
	global_load_dwordx4 v[32:35], v[0:1], off offset:16
	global_load_dwordx4 v[36:39], v[0:1], off
	v_or_b32_e32 v0, 0xa4, v200
	v_mov_b32_e32 v1, v201
	v_lshlrev_b64 v[0:1], 14, v[0:1]
	v_lshl_add_u64 v[0:1], v[6:7], 0, v[0:1]
	global_load_dwordx4 v[40:43], v[0:1], off offset:16
	global_load_dwordx4 v[44:47], v[0:1], off
	v_or_b32_e32 v0, 0xa5, v200
	v_mov_b32_e32 v1, v201
	v_lshlrev_b64 v[0:1], 14, v[0:1]
	v_lshl_add_u64 v[0:1], v[6:7], 0, v[0:1]
	global_load_dwordx4 v[48:51], v[0:1], off offset:16
	global_load_dwordx4 v[52:55], v[0:1], off
	v_or_b32_e32 v0, 0xa6, v200
	v_mov_b32_e32 v1, v201
	v_lshlrev_b64 v[0:1], 14, v[0:1]
	v_lshl_add_u64 v[0:1], v[6:7], 0, v[0:1]
	v_cvt_pk_f16_f32 v117, v60, v68
	v_cvt_pk_f16_f32 v240, v61, v69
	v_cvt_pk_f16_f32 v232, v62, v70
	global_load_dwordx4 v[56:59], v[0:1], off offset:16
	global_load_dwordx4 v[60:63], v[0:1], off
	v_or_b32_e32 v0, 0xa7, v200
	v_mov_b32_e32 v1, v201
	v_lshlrev_b64 v[0:1], 14, v[0:1]
	v_lshl_add_u64 v[0:1], v[6:7], 0, v[0:1]
	global_load_dwordx4 v[64:67], v[0:1], off offset:16
	global_load_dwordx4 v[68:71], v[0:1], off
	v_or_b32_e32 v0, 0xc0, v200
	v_mov_b32_e32 v1, v201
	v_lshlrev_b64 v[0:1], 14, v[0:1]
	v_lshl_add_u64 v[0:1], v[6:7], 0, v[0:1]
	v_accvgpr_write_b32 a19, v117
	v_accvgpr_write_b32 a51, v240
	v_accvgpr_write_b32 a83, v232
	s_waitcnt vmcnt(13)
	v_cvt_pk_f16_f32 v255, v8, v16
	s_waitcnt vmcnt(12)
	v_cvt_pk_f16_f32 v110, v12, v20
	v_cvt_pk_f16_f32 v204, v13, v21
	v_cvt_pk_f16_f32 v251, v9, v17
	v_cvt_pk_f16_f32 v196, v14, v22
	v_cvt_pk_f16_f32 v247, v10, v18
	v_cvt_pk_f16_f32 v212, v15, v23
	v_cvt_pk_f16_f32 v239, v11, v19
	global_load_dwordx4 v[8:11], v[0:1], off offset:16
	global_load_dwordx4 v[12:15], v[0:1], off
	v_or_b32_e32 v0, 0xc1, v200
	v_mov_b32_e32 v1, v201
	v_lshlrev_b64 v[0:1], 14, v[0:1]
	v_lshl_add_u64 v[0:1], v[6:7], 0, v[0:1]
	global_load_dwordx4 v[16:19], v[0:1], off offset:16
	global_load_dwordx4 v[20:23], v[0:1], off
	v_or_b32_e32 v0, 0xc2, v200
	v_mov_b32_e32 v1, v201
	v_lshlrev_b64 v[0:1], 14, v[0:1]
	v_lshl_add_u64 v[0:1], v[6:7], 0, v[0:1]
	s_waitcnt vmcnt(12)
	v_cvt_pk_f16_f32 v111, v28, v36
	v_cvt_pk_f16_f32 v254, v24, v32
	v_cvt_pk_f16_f32 v180, v29, v37
	v_cvt_pk_f16_f32 v250, v25, v33
	v_cvt_pk_f16_f32 v213, v30, v38
	v_cvt_pk_f16_f32 v246, v26, v34
	v_cvt_pk_f16_f32 v216, v31, v39
	v_cvt_pk_f16_f32 v238, v27, v35
	global_load_dwordx4 v[24:27], v[0:1], off offset:16
	global_load_dwordx4 v[28:31], v[0:1], off
	v_or_b32_e32 v0, 0xc3, v200
	v_mov_b32_e32 v1, v201
	v_lshlrev_b64 v[0:1], 14, v[0:1]
	v_lshl_add_u64 v[0:1], v[6:7], 0, v[0:1]
	global_load_dwordx4 v[32:35], v[0:1], off offset:16
	global_load_dwordx4 v[36:39], v[0:1], off
	v_or_b32_e32 v0, 0xc4, v200
	v_mov_b32_e32 v1, v201
	v_lshlrev_b64 v[0:1], 14, v[0:1]
	v_lshl_add_u64 v[0:1], v[6:7], 0, v[0:1]
	s_waitcnt vmcnt(12)
	v_cvt_pk_f16_f32 v112, v44, v52
	v_cvt_pk_f16_f32 v253, v40, v48
	v_cvt_pk_f16_f32 v181, v45, v53
	v_cvt_pk_f16_f32 v249, v41, v49
	v_cvt_pk_f16_f32 v219, v46, v54
	v_cvt_pk_f16_f32 v244, v42, v50
	v_cvt_pk_f16_f32 v218, v47, v55
	v_cvt_pk_f16_f32 v237, v43, v51
	global_load_dwordx4 v[40:43], v[0:1], off offset:16
	global_load_dwordx4 v[44:47], v[0:1], off
	v_or_b32_e32 v0, 0xc5, v200
	v_mov_b32_e32 v1, v201
	v_lshlrev_b64 v[0:1], 14, v[0:1]
	v_lshl_add_u64 v[0:1], v[6:7], 0, v[0:1]
	global_load_dwordx4 v[48:51], v[0:1], off offset:16
	global_load_dwordx4 v[52:55], v[0:1], off
	v_or_b32_e32 v0, 0xc6, v200
	v_mov_b32_e32 v1, v201
	v_lshlrev_b64 v[0:1], 14, v[0:1]
	v_lshl_add_u64 v[0:1], v[6:7], 0, v[0:1]
	s_waitcnt vmcnt(12)
	v_cvt_pk_f16_f32 v113, v60, v68
	v_cvt_pk_f16_f32 v252, v56, v64
	v_cvt_pk_f16_f32 v183, v61, v69
	v_cvt_pk_f16_f32 v248, v57, v65
	v_cvt_pk_f16_f32 v222, v62, v70
	v_cvt_pk_f16_f32 v242, v58, v66
	v_cvt_pk_f16_f32 v221, v63, v71
	v_cvt_pk_f16_f32 v236, v59, v67
	global_load_dwordx4 v[56:59], v[0:1], off offset:16
	global_load_dwordx4 v[60:63], v[0:1], off
	v_or_b32_e32 v0, 0xc7, v200
	v_mov_b32_e32 v1, v201
	v_lshlrev_b64 v[0:1], 14, v[0:1]
	v_lshl_add_u64 v[0:1], v[6:7], 0, v[0:1]
	global_load_dwordx4 v[64:67], v[0:1], off offset:16
	global_load_dwordx4 v[68:71], v[0:1], off
	v_or_b32_e32 v0, 0xe0, v200
	v_mov_b32_e32 v1, v201
	v_lshlrev_b64 v[0:1], 14, v[0:1]
	v_lshl_add_u64 v[0:1], v[6:7], 0, v[0:1]
	v_accvgpr_write_b32 a20, v110
	v_accvgpr_write_b32 a21, v111
	v_accvgpr_write_b32 a22, v112
	v_accvgpr_write_b32 a23, v113
	v_accvgpr_write_b32 a52, v204
	v_accvgpr_write_b32 a53, v180
	v_accvgpr_write_b32 a54, v181
	v_accvgpr_write_b32 a55, v183
	v_accvgpr_write_b32 a84, v196
	v_accvgpr_write_b32 a85, v213
	v_accvgpr_write_b32 a86, v219
	v_accvgpr_write_b32 a87, v222
	v_accvgpr_write_b32 a116, v212
	v_accvgpr_write_b32 a117, v216
	v_accvgpr_write_b32 a118, v218
	v_accvgpr_write_b32 a119, v221
	v_accvgpr_write_b32 a148, v255
	v_accvgpr_write_b32 a149, v254
	v_accvgpr_write_b32 a150, v253
	v_accvgpr_write_b32 a151, v252
	s_waitcnt vmcnt(13)
	v_cvt_pk_f16_f32 v167, v8, v16
	s_waitcnt vmcnt(12)
	v_cvt_pk_f16_f32 v190, v12, v20
	v_cvt_pk_f16_f32 v146, v13, v21
	v_cvt_pk_f16_f32 v171, v9, v17
	v_cvt_pk_f16_f32 v159, v14, v22
	v_cvt_pk_f16_f32 v176, v10, v18
	v_cvt_pk_f16_f32 v163, v15, v23
	v_cvt_pk_f16_f32 v189, v11, v19
	global_load_dwordx4 v[8:11], v[0:1], off offset:16
	global_load_dwordx4 v[12:15], v[0:1], off
	v_or_b32_e32 v0, 0xe1, v200
	v_mov_b32_e32 v1, v201
	v_lshlrev_b64 v[0:1], 14, v[0:1]
	v_lshl_add_u64 v[0:1], v[6:7], 0, v[0:1]
	global_load_dwordx4 v[16:19], v[0:1], off offset:16
	global_load_dwordx4 v[20:23], v[0:1], off
	v_or_b32_e32 v0, 0xe2, v200
	v_mov_b32_e32 v1, v201
	v_lshlrev_b64 v[0:1], 14, v[0:1]
	v_lshl_add_u64 v[0:1], v[6:7], 0, v[0:1]
	s_waitcnt vmcnt(13)
	v_cvt_pk_f16_f32 v168, v24, v32
	s_waitcnt vmcnt(12)
	v_cvt_pk_f16_f32 v224, v28, v36
	v_cvt_pk_f16_f32 v147, v29, v37
	v_cvt_pk_f16_f32 v172, v25, v33
	v_cvt_pk_f16_f32 v160, v30, v38
	v_cvt_pk_f16_f32 v177, v26, v34
	v_cvt_pk_f16_f32 v164, v31, v39
	v_cvt_pk_f16_f32 v191, v27, v35
	global_load_dwordx4 v[24:27], v[0:1], off offset:16
	global_load_dwordx4 v[28:31], v[0:1], off
	v_or_b32_e32 v0, 0xe3, v200
	v_mov_b32_e32 v1, v201
	v_lshlrev_b64 v[0:1], 14, v[0:1]
	v_lshl_add_u64 v[0:1], v[6:7], 0, v[0:1]
	global_load_dwordx4 v[32:35], v[0:1], off offset:16
	global_load_dwordx4 v[36:39], v[0:1], off
	v_or_b32_e32 v0, 0xe4, v200
	v_mov_b32_e32 v1, v201
	v_lshlrev_b64 v[0:1], 14, v[0:1]
	v_lshl_add_u64 v[0:1], v[6:7], 0, v[0:1]
	s_waitcnt vmcnt(13)
	v_cvt_pk_f16_f32 v169, v40, v48
	s_waitcnt vmcnt(12)
	v_cvt_pk_f16_f32 v223, v44, v52
	v_cvt_pk_f16_f32 v148, v45, v53
	v_cvt_pk_f16_f32 v174, v41, v49
	v_cvt_pk_f16_f32 v161, v46, v54
	v_cvt_pk_f16_f32 v178, v42, v50
	v_cvt_pk_f16_f32 v165, v47, v55
	v_cvt_pk_f16_f32 v192, v43, v51
	global_load_dwordx4 v[40:43], v[0:1], off offset:16
	global_load_dwordx4 v[44:47], v[0:1], off
	v_or_b32_e32 v0, 0xe5, v200
	v_mov_b32_e32 v1, v201
	v_lshlrev_b64 v[0:1], 14, v[0:1]
	v_lshl_add_u64 v[0:1], v[6:7], 0, v[0:1]
	global_load_dwordx4 v[48:51], v[0:1], off offset:16
	global_load_dwordx4 v[52:55], v[0:1], off
	v_or_b32_e32 v0, 0xe6, v200
	v_mov_b32_e32 v1, v201
	v_lshlrev_b64 v[0:1], 14, v[0:1]
	v_lshl_add_u64 v[0:1], v[6:7], 0, v[0:1]
	v_or_b32_e32 v200, 0xe7, v200
	s_waitcnt vmcnt(12)
	v_cvt_pk_f16_f32 v194, v60, v68
	v_cvt_pk_f16_f32 v170, v56, v64
	v_cvt_pk_f16_f32 v149, v61, v69
	v_cvt_pk_f16_f32 v175, v57, v65
	v_cvt_pk_f16_f32 v162, v62, v70
	v_cvt_pk_f16_f32 v179, v58, v66
	v_cvt_pk_f16_f32 v166, v63, v71
	v_cvt_pk_f16_f32 v195, v59, v67
	global_load_dwordx4 v[56:59], v[0:1], off offset:16
	global_load_dwordx4 v[60:63], v[0:1], off
	v_lshlrev_b64 v[0:1], 14, v[200:201]
	v_lshl_add_u64 v[0:1], v[6:7], 0, v[0:1]
	global_load_dwordx4 v[64:67], v[0:1], off offset:16
	global_load_dwordx4 v[68:71], v[0:1], off
	v_or_b32_e32 v200, s14, v217
	v_lshlrev_b64 v[0:1], 14, v[200:201]
	v_accvgpr_write_b32 a24, v190
	v_accvgpr_write_b32 a25, v224
	v_accvgpr_write_b32 a26, v223
	v_accvgpr_write_b32 a27, v194
	v_accvgpr_write_b32 a56, v146
	v_accvgpr_write_b32 a57, v147
	v_accvgpr_write_b32 a58, v148
	v_accvgpr_write_b32 a59, v149
	v_accvgpr_write_b32 a88, v159
	v_accvgpr_write_b32 a89, v160
	v_accvgpr_write_b32 a90, v161
	v_accvgpr_write_b32 a91, v162
	v_accvgpr_write_b32 a120, v163
	v_accvgpr_write_b32 a121, v164
	v_accvgpr_write_b32 a122, v165
	v_accvgpr_write_b32 a123, v166
	v_accvgpr_write_b32 a152, v167
	v_accvgpr_write_b32 a153, v168
	v_accvgpr_write_b32 a154, v169
	v_accvgpr_write_b32 a155, v170
	v_accvgpr_write_b32 a180, v251
	v_accvgpr_write_b32 a181, v250
	v_accvgpr_write_b32 a182, v249
	s_waitcnt vmcnt(13)
	v_cvt_pk_f16_f32 v134, v8, v16
	v_cvt_pk_f16_f32 v138, v9, v17
	v_cvt_pk_f16_f32 v142, v10, v18
	v_cvt_pk_f16_f32 v151, v11, v19
	s_waitcnt vmcnt(12)
	v_cvt_pk_f16_f32 v173, v12, v20
	v_cvt_pk_f16_f32 v118, v13, v21
	v_cvt_pk_f16_f32 v126, v14, v22
	v_cvt_pk_f16_f32 v130, v15, v23
	v_accvgpr_write_b32 a28, v173
	v_accvgpr_write_b32 a60, v118
	v_accvgpr_write_b32 a92, v126
	v_accvgpr_write_b32 a124, v130
	v_accvgpr_write_b32 a156, v134
	v_accvgpr_write_b32 a183, v248
	v_accvgpr_write_b32 a184, v171
	v_accvgpr_write_b32 a185, v172
	v_accvgpr_write_b32 a186, v174
	v_accvgpr_write_b32 a187, v175
	s_waitcnt vmcnt(9)
	v_cvt_pk_f16_f32 v135, v24, v32
	v_cvt_pk_f16_f32 v139, v25, v33
	v_cvt_pk_f16_f32 v143, v26, v34
	v_cvt_pk_f16_f32 v152, v27, v35
	s_waitcnt vmcnt(8)
	v_cvt_pk_f16_f32 v182, v28, v36
	v_cvt_pk_f16_f32 v119, v29, v37
	v_cvt_pk_f16_f32 v127, v30, v38
	v_cvt_pk_f16_f32 v131, v31, v39
	v_accvgpr_write_b32 a29, v182
	v_accvgpr_write_b32 a61, v119
	v_accvgpr_write_b32 a93, v127
	v_accvgpr_write_b32 a125, v131
	v_accvgpr_write_b32 a157, v135
	v_accvgpr_write_b32 a188, v138
	v_accvgpr_write_b32 a189, v139
	v_accvgpr_write_b32 a212, v247
	v_accvgpr_write_b32 a213, v246
	v_accvgpr_write_b32 a214, v244
	s_waitcnt vmcnt(5)
	v_cvt_pk_f16_f32 v136, v40, v48
	v_cvt_pk_f16_f32 v140, v41, v49
	v_cvt_pk_f16_f32 v144, v42, v50
	v_cvt_pk_f16_f32 v153, v43, v51
	s_waitcnt vmcnt(4)
	v_cvt_pk_f16_f32 v184, v44, v52
	v_cvt_pk_f16_f32 v120, v45, v53
	v_cvt_pk_f16_f32 v128, v46, v54
	v_cvt_pk_f16_f32 v132, v47, v55
	v_accvgpr_write_b32 a30, v184
	v_accvgpr_write_b32 a62, v120
	v_accvgpr_write_b32 a94, v128
	v_accvgpr_write_b32 a126, v132
	v_accvgpr_write_b32 a158, v136
	v_accvgpr_write_b32 a190, v140
	v_accvgpr_write_b32 a215, v242
	v_accvgpr_write_b32 a216, v176
	v_accvgpr_write_b32 a217, v177
	s_waitcnt vmcnt(1)
	v_cvt_pk_f16_f32 v137, v56, v64
	v_cvt_pk_f16_f32 v141, v57, v65
	v_lshl_add_u64 v[64:65], s[12:13], 0, v[4:5]
	v_lshl_add_u64 v[0:1], v[64:65], 0, v[0:1]
	global_load_dwordx4 v[4:7], v[0:1], off offset:16
	global_load_dwordx4 v[8:11], v[0:1], off
	v_or_b32_e32 v0, 1, v200
	v_mov_b32_e32 v1, v201
	v_lshlrev_b64 v[0:1], 14, v[0:1]
	v_lshl_add_u64 v[0:1], v[64:65], 0, v[0:1]
	global_load_dwordx4 v[12:15], v[0:1], off offset:16
	global_load_dwordx4 v[16:19], v[0:1], off
	v_or_b32_e32 v0, 2, v200
	v_mov_b32_e32 v1, v201
	v_lshlrev_b64 v[0:1], 14, v[0:1]
	v_lshl_add_u64 v[0:1], v[64:65], 0, v[0:1]
	global_load_dwordx4 v[20:23], v[0:1], off offset:16
	global_load_dwordx4 v[24:27], v[0:1], off
	v_or_b32_e32 v0, 3, v200
	v_mov_b32_e32 v1, v201
	v_lshlrev_b64 v[0:1], 14, v[0:1]
	v_lshl_add_u64 v[0:1], v[64:65], 0, v[0:1]
	global_load_dwordx4 v[28:31], v[0:1], off offset:16
	global_load_dwordx4 v[32:35], v[0:1], off
	v_or_b32_e32 v0, 4, v200
	v_mov_b32_e32 v1, v201
	v_lshlrev_b64 v[0:1], 14, v[0:1]
	v_lshl_add_u64 v[0:1], v[64:65], 0, v[0:1]
	global_load_dwordx4 v[36:39], v[0:1], off offset:16
	global_load_dwordx4 v[40:43], v[0:1], off
	v_or_b32_e32 v0, 5, v200
	v_mov_b32_e32 v1, v201
	v_lshlrev_b64 v[0:1], 14, v[0:1]
	v_lshl_add_u64 v[0:1], v[64:65], 0, v[0:1]
	global_load_dwordx4 v[44:47], v[0:1], off offset:16
	global_load_dwordx4 v[48:51], v[0:1], off
	v_or_b32_e32 v0, 6, v200
	v_mov_b32_e32 v1, v201
	v_lshlrev_b64 v[0:1], 14, v[0:1]
	v_lshl_add_u64 v[0:1], v[64:65], 0, v[0:1]
	v_cvt_pk_f16_f32 v145, v58, v66
	v_cvt_pk_f16_f32 v154, v59, v67
	global_load_dwordx4 v[52:55], v[0:1], off offset:16
	global_load_dwordx4 v[56:59], v[0:1], off
	v_or_b32_e32 v0, 7, v200
	v_mov_b32_e32 v1, v201
	v_lshlrev_b64 v[0:1], 14, v[0:1]
	v_lshl_add_u64 v[0:1], v[64:65], 0, v[0:1]
	s_waitcnt vmcnt(14)
	v_cvt_pk_f16_f32 v209, v60, v68
	v_cvt_pk_f16_f32 v121, v61, v69
	v_cvt_pk_f16_f32 v129, v62, v70
	v_cvt_pk_f16_f32 v133, v63, v71
	global_load_dwordx4 v[60:63], v[0:1], off offset:16
	global_load_dwordx4 v[66:69], v[0:1], off
	v_or_b32_e32 v0, 32, v200
	v_mov_b32_e32 v1, v201
	v_lshlrev_b64 v[0:1], 14, v[0:1]
	v_lshl_add_u64 v[0:1], v[64:65], 0, v[0:1]
	v_readfirstlane_b32 s12, v186
	s_lshl_b32 s13, s19, 3
	v_or_b32_e32 v214, s13, v150
	v_ashrrev_i32_e32 v215, 31, v214
	v_accvgpr_write_b32 a31, v209
	v_accvgpr_write_b32 a63, v121
	v_accvgpr_write_b32 a95, v129
	v_accvgpr_write_b32 a127, v133
	v_accvgpr_write_b32 a159, v137
	v_accvgpr_write_b32 a191, v141
	v_accvgpr_write_b32 a218, v178
	v_accvgpr_write_b32 a219, v179
	v_accvgpr_write_b32 a220, v142
	v_accvgpr_write_b32 a221, v143
	v_accvgpr_write_b32 a222, v144
	v_accvgpr_write_b32 a223, v145
	v_accvgpr_write_b32 a244, v239
	v_accvgpr_write_b32 a245, v238
	v_accvgpr_write_b32 a246, v237
	v_accvgpr_write_b32 a247, v236
	v_accvgpr_write_b32 a248, v189
	v_accvgpr_write_b32 a249, v191
	v_accvgpr_write_b32 a250, v192
	v_accvgpr_write_b32 a251, v195
	v_accvgpr_write_b32 a252, v151
	v_accvgpr_write_b32 a253, v152
	v_accvgpr_write_b32 a254, v153
	v_accvgpr_write_b32 a255, v154
	s_waitcnt vmcnt(13)
	v_cvt_pk_f16_f32 v74, v4, v12
	s_waitcnt vmcnt(12)
	v_cvt_pk_f16_f32 v70, v8, v16
	v_cvt_pk_f16_f32 v78, v9, v17
	v_cvt_pk_f16_f32 v82, v5, v13
	v_cvt_pk_f16_f32 v86, v10, v18
	v_cvt_pk_f16_f32 v2, v6, v14
	v_cvt_pk_f16_f32 v8, v7, v15
	s_waitcnt vmcnt(9)
	v_cvt_pk_f16_f32 v75, v20, v28
	s_waitcnt vmcnt(8)
	v_cvt_pk_f16_f32 v71, v24, v32
	v_cvt_pk_f16_f32 v79, v25, v33
	v_cvt_pk_f16_f32 v83, v21, v29
	v_cvt_pk_f16_f32 v87, v26, v34
	v_cvt_pk_f16_f32 v3, v22, v30
	v_cvt_pk_f16_f32 v27, v27, v35
	v_cvt_pk_f16_f32 v26, v11, v19
	v_cvt_pk_f16_f32 v9, v23, v31
	s_waitcnt vmcnt(5)
	v_cvt_pk_f16_f32 v76, v36, v44
	s_waitcnt vmcnt(4)
	v_cvt_pk_f16_f32 v72, v40, v48
	v_cvt_pk_f16_f32 v80, v41, v49
	v_cvt_pk_f16_f32 v84, v37, v45
	v_cvt_pk_f16_f32 v88, v42, v50
	v_cvt_pk_f16_f32 v4, v38, v46
	v_cvt_pk_f16_f32 v28, v43, v51
	v_cvt_pk_f16_f32 v10, v39, v47
	s_waitcnt vmcnt(1)
	v_cvt_pk_f16_f32 v77, v52, v60
	s_waitcnt vmcnt(0)
	v_cvt_pk_f16_f32 v73, v56, v66
	v_cvt_pk_f16_f32 v81, v57, v67
	v_cvt_pk_f16_f32 v85, v53, v61
	v_cvt_pk_f16_f32 v89, v58, v68
	v_cvt_pk_f16_f32 v5, v54, v62
	v_cvt_pk_f16_f32 v29, v59, v69
	v_cvt_pk_f16_f32 v11, v55, v63
	ds_write_b128 v95, v[70:73]
	ds_write_b128 v95, v[78:81] offset:1024
	ds_write_b128 v95, v[86:89] offset:2048
	ds_write_b128 v95, v[26:29] offset:3072
	ds_write_b128 v95, v[74:77] offset:4096
	ds_write_b128 v95, v[82:85] offset:5120
	ds_write_b128 v95, v[2:5] offset:6144
	ds_write_b128 v95, v[8:11] offset:7168
	global_load_dwordx4 v[4:7], v[0:1], off offset:16
	global_load_dwordx4 v[12:15], v[0:1], off
	v_or_b32_e32 v0, 33, v200
	v_mov_b32_e32 v1, v201
	v_lshlrev_b64 v[0:1], 14, v[0:1]
	v_lshl_add_u64 v[0:1], v[64:65], 0, v[0:1]
	global_load_dwordx4 v[8:11], v[0:1], off offset:16
	global_load_dwordx4 v[16:19], v[0:1], off
	v_or_b32_e32 v0, 34, v200
	v_mov_b32_e32 v1, v201
	v_lshlrev_b64 v[0:1], 14, v[0:1]
	v_lshl_add_u64 v[0:1], v[64:65], 0, v[0:1]
	global_load_dwordx4 v[20:23], v[0:1], off offset:16
	global_load_dwordx4 v[32:35], v[0:1], off
	v_or_b32_e32 v0, 35, v200
	v_mov_b32_e32 v1, v201
	v_lshlrev_b64 v[0:1], 14, v[0:1]
	v_lshl_add_u64 v[0:1], v[64:65], 0, v[0:1]
	global_load_dwordx4 v[24:27], v[0:1], off offset:16
	global_load_dwordx4 v[40:43], v[0:1], off
	v_or_b32_e32 v0, 36, v200
	v_mov_b32_e32 v1, v201
	v_lshlrev_b64 v[0:1], 14, v[0:1]
	v_lshl_add_u64 v[0:1], v[64:65], 0, v[0:1]
	global_load_dwordx4 v[28:31], v[0:1], off offset:16
	global_load_dwordx4 v[44:47], v[0:1], off
	v_or_b32_e32 v0, 37, v200
	v_mov_b32_e32 v1, v201
	v_lshlrev_b64 v[0:1], 14, v[0:1]
	v_lshl_add_u64 v[0:1], v[64:65], 0, v[0:1]
	global_load_dwordx4 v[36:39], v[0:1], off offset:16
	global_load_dwordx4 v[48:51], v[0:1], off
	v_or_b32_e32 v0, 38, v200
	v_mov_b32_e32 v1, v201
	v_lshlrev_b64 v[0:1], 14, v[0:1]
	v_lshl_add_u64 v[0:1], v[64:65], 0, v[0:1]
	global_load_dwordx4 v[52:55], v[0:1], off offset:16
	global_load_dwordx4 v[56:59], v[0:1], off
	v_or_b32_e32 v0, 39, v200
	v_mov_b32_e32 v1, v201
	v_lshlrev_b64 v[0:1], 14, v[0:1]
	v_lshl_add_u64 v[0:1], v[64:65], 0, v[0:1]
	global_load_dwordx4 v[60:63], v[0:1], off offset:16
	global_load_dwordx4 v[66:69], v[0:1], off
	v_or_b32_e32 v0, s0, v193
	v_lshlrev_b32_e32 v94, 4, v0
	v_or_b32_e32 v0, 0x3c00, v94
	v_mov_b32_e32 v1, v201
	v_bfe_u32 v193, v193, 3, 1
	v_cmp_gt_u32_e64 s[0:1], 8, v220
	s_waitcnt vmcnt(13)
	v_cvt_pk_f16_f32 v74, v4, v8
	s_waitcnt vmcnt(12)
	v_cvt_pk_f16_f32 v70, v12, v16
	v_cvt_pk_f16_f32 v78, v13, v17
	v_cvt_pk_f16_f32 v2, v14, v18
	v_cvt_pk_f16_f32 v12, v7, v11
	v_cvt_pk_f16_f32 v82, v5, v9
	v_cvt_pk_f16_f32 v86, v6, v10
	s_waitcnt vmcnt(9)
	v_cvt_pk_f16_f32 v13, v23, v27
	s_waitcnt vmcnt(8)
	v_cvt_pk_f16_f32 v71, v32, v40
	v_cvt_pk_f16_f32 v3, v34, v42
	v_cvt_pk_f16_f32 v34, v15, v19
	v_cvt_pk_f16_f32 v75, v20, v24
	v_cvt_pk_f16_f32 v79, v33, v41
	v_cvt_pk_f16_f32 v83, v21, v25
	v_cvt_pk_f16_f32 v87, v22, v26
	v_cvt_pk_f16_f32 v35, v35, v43
	s_waitcnt vmcnt(5)
	v_cvt_pk_f16_f32 v14, v31, v39
	s_waitcnt vmcnt(4)
	v_cvt_pk_f16_f32 v72, v44, v48
	v_cvt_pk_f16_f32 v76, v28, v36
	v_cvt_pk_f16_f32 v80, v45, v49
	v_cvt_pk_f16_f32 v84, v29, v37
	v_cvt_pk_f16_f32 v4, v46, v50
	v_cvt_pk_f16_f32 v88, v30, v38
	v_cvt_pk_f16_f32 v36, v47, v51
	s_waitcnt vmcnt(1)
	v_cvt_pk_f16_f32 v15, v55, v63
	s_waitcnt vmcnt(0)
	v_cvt_pk_f16_f32 v73, v56, v66
	v_cvt_pk_f16_f32 v77, v52, v60
	v_cvt_pk_f16_f32 v81, v57, v67
	v_cvt_pk_f16_f32 v85, v53, v61
	v_cvt_pk_f16_f32 v5, v58, v68
	v_cvt_pk_f16_f32 v89, v54, v62
	v_cvt_pk_f16_f32 v37, v59, v69
	ds_write_b128 v95, v[70:73] offset:8192
	ds_write_b128 v95, v[78:81] offset:9216
	ds_write_b128 v95, v[2:5] offset:10240
	ds_write_b128 v95, v[34:37] offset:11264
	ds_write_b128 v95, v[74:77] offset:12288
	ds_write_b128 v95, v[82:85] offset:13312
	ds_write_b128 v95, v[86:89] offset:14336
	ds_write_b128 v0, v[12:15]
	v_or_b32_e32 v0, 64, v200
	v_lshlrev_b64 v[0:1], 14, v[0:1]
	v_lshl_add_u64 v[0:1], v[64:65], 0, v[0:1]
	global_load_dwordx4 v[4:7], v[0:1], off offset:16
	global_load_dwordx4 v[8:11], v[0:1], off
	v_or_b32_e32 v0, 0x41, v200
	v_mov_b32_e32 v1, v201
	v_lshlrev_b64 v[0:1], 14, v[0:1]
	v_lshl_add_u64 v[0:1], v[64:65], 0, v[0:1]
	global_load_dwordx4 v[12:15], v[0:1], off offset:16
	global_load_dwordx4 v[16:19], v[0:1], off
	v_or_b32_e32 v0, 0x42, v200
	v_mov_b32_e32 v1, v201
	v_lshlrev_b64 v[0:1], 14, v[0:1]
	v_lshl_add_u64 v[0:1], v[64:65], 0, v[0:1]
	global_load_dwordx4 v[20:23], v[0:1], off offset:16
	global_load_dwordx4 v[28:31], v[0:1], off
	v_or_b32_e32 v0, 0x43, v200
	v_mov_b32_e32 v1, v201
	v_lshlrev_b64 v[0:1], 14, v[0:1]
	v_lshl_add_u64 v[0:1], v[64:65], 0, v[0:1]
	global_load_dwordx4 v[24:27], v[0:1], off offset:16
	global_load_dwordx4 v[32:35], v[0:1], off
	v_or_b32_e32 v0, 0x44, v200
	v_mov_b32_e32 v1, v201
	v_lshlrev_b64 v[0:1], 14, v[0:1]
	v_lshl_add_u64 v[0:1], v[64:65], 0, v[0:1]
	global_load_dwordx4 v[36:39], v[0:1], off offset:16
	global_load_dwordx4 v[40:43], v[0:1], off
	v_or_b32_e32 v0, 0x45, v200
	v_mov_b32_e32 v1, v201
	v_lshlrev_b64 v[0:1], 14, v[0:1]
	v_lshl_add_u64 v[0:1], v[64:65], 0, v[0:1]
	global_load_dwordx4 v[44:47], v[0:1], off offset:16
	global_load_dwordx4 v[48:51], v[0:1], off
	v_or_b32_e32 v0, 0x46, v200
	v_mov_b32_e32 v1, v201
	v_lshlrev_b64 v[0:1], 14, v[0:1]
	v_lshl_add_u64 v[0:1], v[64:65], 0, v[0:1]
	global_load_dwordx4 v[52:55], v[0:1], off offset:16
	global_load_dwordx4 v[56:59], v[0:1], off
	v_or_b32_e32 v0, 0x47, v200
	v_mov_b32_e32 v1, v201
	v_lshlrev_b64 v[0:1], 14, v[0:1]
	v_lshl_add_u64 v[0:1], v[64:65], 0, v[0:1]
	global_load_dwordx4 v[60:63], v[0:1], off offset:16
	global_load_dwordx4 v[66:69], v[0:1], off
	v_or_b32_e32 v0, 0x60, v200
	v_mov_b32_e32 v1, v201
	v_lshlrev_b64 v[0:1], 14, v[0:1]
	v_lshl_add_u64 v[0:1], v[64:65], 0, v[0:1]
	s_waitcnt vmcnt(13)
	v_cvt_pk_f16_f32 v74, v4, v12
	s_waitcnt vmcnt(12)
	v_cvt_pk_f16_f32 v70, v8, v16
	v_cvt_pk_f16_f32 v78, v9, v17
	v_cvt_pk_f16_f32 v82, v5, v13
	v_cvt_pk_f16_f32 v2, v10, v18
	v_cvt_pk_f16_f32 v86, v6, v14
	v_cvt_pk_f16_f32 v8, v7, v15
	s_waitcnt vmcnt(9)
	v_cvt_pk_f16_f32 v75, v20, v24
	s_waitcnt vmcnt(8)
	v_cvt_pk_f16_f32 v71, v28, v32
	v_cvt_pk_f16_f32 v79, v29, v33
	v_cvt_pk_f16_f32 v83, v21, v25
	v_cvt_pk_f16_f32 v3, v30, v34
	v_cvt_pk_f16_f32 v87, v22, v26
	v_cvt_pk_f16_f32 v31, v31, v35
	v_cvt_pk_f16_f32 v30, v11, v19
	v_cvt_pk_f16_f32 v9, v23, v27
	s_waitcnt vmcnt(5)
	v_cvt_pk_f16_f32 v76, v36, v44
	s_waitcnt vmcnt(4)
	v_cvt_pk_f16_f32 v72, v40, v48
	v_cvt_pk_f16_f32 v80, v41, v49
	v_cvt_pk_f16_f32 v84, v37, v45
	v_cvt_pk_f16_f32 v4, v42, v50
	v_cvt_pk_f16_f32 v88, v38, v46
	v_cvt_pk_f16_f32 v32, v43, v51
	v_cvt_pk_f16_f32 v10, v39, v47
	s_waitcnt vmcnt(1)
	v_cvt_pk_f16_f32 v77, v52, v60
	s_waitcnt vmcnt(0)
	v_cvt_pk_f16_f32 v73, v56, v66
	v_cvt_pk_f16_f32 v81, v57, v67
	v_cvt_pk_f16_f32 v85, v53, v61
	v_cvt_pk_f16_f32 v5, v58, v68
	v_cvt_pk_f16_f32 v89, v54, v62
	v_cvt_pk_f16_f32 v33, v59, v69
	v_cvt_pk_f16_f32 v11, v55, v63
	ds_write_b128 v95, v[70:73] offset:16384
	ds_write_b128 v95, v[78:81] offset:17408
	ds_write_b128 v95, v[2:5] offset:18432
	ds_write_b128 v95, v[30:33] offset:19456
	ds_write_b128 v95, v[74:77] offset:20480
	ds_write_b128 v95, v[82:85] offset:21504
	ds_write_b128 v95, v[86:89] offset:22528
	ds_write_b128 v95, v[8:11] offset:23552
	global_load_dwordx4 v[8:11], v[0:1], off offset:16
	global_load_dwordx4 v[40:43], v[0:1], off
	v_or_b32_e32 v0, 0x61, v200
	v_mov_b32_e32 v1, v201
	v_lshlrev_b64 v[0:1], 14, v[0:1]
	v_lshl_add_u64 v[0:1], v[64:65], 0, v[0:1]
	global_load_dwordx4 v[16:19], v[0:1], off offset:16
	global_load_dwordx4 v[48:51], v[0:1], off
	v_or_b32_e32 v0, 0x62, v200
	v_mov_b32_e32 v1, v201
	v_lshlrev_b64 v[0:1], 14, v[0:1]
	v_lshl_add_u64 v[0:1], v[64:65], 0, v[0:1]
	global_load_dwordx4 v[30:33], v[0:1], off offset:16
	global_load_dwordx4 v[56:59], v[0:1], off
	v_or_b32_e32 v0, 0x63, v200
	v_mov_b32_e32 v1, v201
	v_lshlrev_b64 v[0:1], 14, v[0:1]
	v_lshl_add_u64 v[0:1], v[64:65], 0, v[0:1]
	global_load_dwordx4 v[34:37], v[0:1], off offset:16
	global_load_dwordx4 v[60:63], v[0:1], off
	v_or_b32_e32 v0, 0x64, v200
	v_mov_b32_e32 v1, v201
	v_lshlrev_b64 v[0:1], 14, v[0:1]
	v_lshl_add_u64 v[0:1], v[64:65], 0, v[0:1]
	global_load_dwordx4 v[44:47], v[0:1], off offset:16
	global_load_dwordx4 v[72:75], v[0:1], off
	v_or_b32_e32 v0, 0x65, v200
	v_mov_b32_e32 v1, v201
	v_lshlrev_b64 v[0:1], 14, v[0:1]
	v_lshl_add_u64 v[0:1], v[64:65], 0, v[0:1]
	global_load_dwordx4 v[52:55], v[0:1], off offset:16
	global_load_dwordx4 v[80:83], v[0:1], off
	v_or_b32_e32 v0, 0x66, v200
	v_mov_b32_e32 v1, v201
	v_lshlrev_b64 v[0:1], 14, v[0:1]
	v_lshl_add_u64 v[0:1], v[64:65], 0, v[0:1]
	v_or_b32_e32 v200, 0x67, v200
	global_load_dwordx4 v[68:71], v[0:1], off offset:16
	global_load_dwordx4 v[84:87], v[0:1], off
	v_lshlrev_b64 v[0:1], 14, v[200:201]
	v_lshl_add_u64 v[0:1], v[64:65], 0, v[0:1]
	global_load_dwordx4 v[76:79], v[0:1], off offset:16
	s_nop 0
	global_load_dwordx4 v[0:3], v[0:1], off
	v_lshlrev_b32_e32 v200, 5, v109
	s_waitcnt vmcnt(13)
	v_cvt_pk_f16_f32 v4, v8, v16
	s_waitcnt vmcnt(12)
	v_cvt_pk_f16_f32 v64, v40, v48
	v_cvt_pk_f16_f32 v20, v41, v49
	v_cvt_pk_f16_f32 v12, v9, v17
	v_cvt_pk_f16_f32 v28, v42, v50
	v_cvt_pk_f16_f32 v24, v10, v18
	v_cvt_pk_f16_f32 v38, v43, v51
	s_waitcnt vmcnt(9)
	v_cvt_pk_f16_f32 v5, v30, v34
	s_waitcnt vmcnt(8)
	v_cvt_pk_f16_f32 v65, v56, v60
	v_cvt_pk_f16_f32 v13, v31, v35
	v_cvt_pk_f16_f32 v25, v32, v36
	v_cvt_pk_f16_f32 v33, v33, v37
	v_cvt_pk_f16_f32 v32, v11, v19
	v_cvt_pk_f16_f32 v21, v57, v61
	v_cvt_pk_f16_f32 v29, v58, v62
	v_cvt_pk_f16_f32 v39, v59, v63
	s_waitcnt vmcnt(5)
	v_cvt_pk_f16_f32 v26, v46, v54
	v_add_u32_e32 v54, s2, v208
	s_waitcnt vmcnt(4)
	v_cvt_pk_f16_f32 v66, v72, v80
	v_cvt_pk_f16_f32 v34, v47, v55
	v_ashrrev_i32_e32 v55, 31, v54
	v_cvt_pk_f16_f32 v6, v44, v52
	v_cvt_pk_f16_f32 v22, v73, v81
	v_cvt_pk_f16_f32 v14, v45, v53
	v_cvt_pk_f16_f32 v30, v74, v82
	s_waitcnt vmcnt(1)
	v_cvt_pk_f16_f32 v35, v71, v79
	s_waitcnt vmcnt(0)
	v_cvt_pk_f16_f32 v67, v84, v0
	v_or_b32_e32 v0, 0x7c00, v94
	v_cvt_pk_f16_f32 v7, v68, v76
	v_cvt_pk_f16_f32 v23, v85, v1
	v_cvt_pk_f16_f32 v15, v69, v77
	v_cvt_pk_f16_f32 v31, v86, v2
	v_cvt_pk_f16_f32 v27, v70, v78
	v_cvt_pk_f16_f32 v41, v87, v3
	v_cvt_pk_f16_f32 v40, v75, v83
	ds_write_b128 v95, v[64:67] offset:24576
	ds_write_b128 v95, v[20:23] offset:25600
	ds_write_b128 v95, v[28:31] offset:26624
	ds_write_b128 v95, v[38:41] offset:27648
	ds_write_b128 v95, v[4:7] offset:28672
	ds_write_b128 v95, v[12:15] offset:29696
	ds_write_b128 v95, v[24:27] offset:30720
	ds_write_b128 v0, v[32:35]
	v_lshl_add_u64 v[0:1], v[54:55], 2, s[4:5]
	global_load_dword v185, v[0:1], off
	v_add_u32_e32 v0, 0x400, v54
	v_ashrrev_i32_e32 v1, 31, v0
	v_lshl_add_u64 v[0:1], v[0:1], 2, s[4:5]
	global_load_dword v186, v[0:1], off
	v_add_u32_e32 v0, 0x800, v54
	v_ashrrev_i32_e32 v1, 31, v0
	v_lshl_add_u64 v[0:1], v[0:1], 2, s[4:5]
	global_load_dword v187, v[0:1], off
	v_add_u32_e32 v0, 0xc00, v54
	v_ashrrev_i32_e32 v1, 31, v0
	v_lshl_add_u64 v[0:1], v[0:1], 2, s[4:5]
	global_load_dword v188, v[0:1], off
	v_lshlrev_b64 v[0:1], 20, v[214:215]
	v_lshl_add_u64 v[0:1], s[16:17], 0, v[0:1]
	v_lshl_add_u64 v[0:1], s[14:15], 2, v[0:1]
	v_lshl_add_u64 v[210:211], v[0:1], 0, v[200:201]
	global_load_dwordx4 v[4:7], v[210:211], off offset:256
	global_load_dwordx4 v[8:11], v[210:211], off offset:272
	global_load_dwordx4 v[14:17], v[210:211], off offset:384
	global_load_dwordx4 v[18:21], v[210:211], off offset:400
	v_lshlrev_b32_e32 v0, 4, v198
	s_waitcnt lgkmcnt(0)
	s_barrier
	ds_read_b128 v[96:99], v0 offset:23552
	ds_read_b128 v[92:95], v0 offset:22528
	ds_read_b128 v[88:91], v0 offset:21504
	ds_read_b128 v[60:63], v0 offset:20480
	ds_read_b128 v[64:67], v0 offset:19456
	ds_read_b128 v[68:71], v0 offset:18432
	ds_read_b128 v[72:75], v0 offset:17408
	ds_read_b128 v[76:79], v0 offset:16384
	v_mov_b64_e32 v[44:45], s[26:27]
	v_mov_b64_e32 v[40:41], s[26:27]
	v_mov_b64_e32 v[22:23], s[24:25]
	v_mov_b64_e32 v[28:29], s[26:27]
	v_mov_b64_e32 v[32:33], s[26:27]
	v_mov_b64_e32 v[36:37], s[26:27]
	v_mov_b64_e32 v[42:43], s[24:25]
	v_mov_b64_e32 v[38:39], s[24:25]
	v_mov_b64_e32 v[24:25], s[26:27]
	v_mov_b64_e32 v[26:27], s[24:25]
	v_mov_b64_e32 v[30:31], s[24:25]
	v_mov_b64_e32 v[34:35], s[24:25]
	s_or_b32 s4, s3, s13
	s_ashr_i32 s5, s4, 31
	s_lshl_b64 s[4:5], s[4:5], 20
	s_add_u32 s4, s16, s4
	s_addc_u32 s5, s17, s5
	s_cmp_lg_u32 s12, 0
	v_mov_b32_e32 v200, v201
	s_waitcnt vmcnt(3)
	v_cvt_pk_f16_f32 v101, v6, v7
	s_waitcnt vmcnt(2)
	v_cvt_pk_f16_f32 v103, v10, v11
	v_cvt_pk_f16_f32 v102, v8, v9
	v_cvt_pk_f16_f32 v100, v4, v5
	ds_read_b128 v[80:83], v0 offset:31744
	ds_read_b128 v[84:87], v0 offset:30720
	ds_read_b128 v[56:59], v0 offset:29696
	ds_read_b128 v[50:53], v0 offset:28672
	ds_read_b128 v[46:49], v0 offset:27648
	ds_read_b128 v[8:11], v0 offset:26624
	ds_read_b128 v[4:7], v0 offset:25600
	ds_read_b128 v[0:3], v0 offset:24576
	s_waitcnt vmcnt(0)
	v_cvt_pk_f16_f32 v107, v20, v21
	v_cvt_pk_f16_f32 v106, v18, v19
	v_cvt_pk_f16_f32 v105, v16, v17
	v_cvt_pk_f16_f32 v104, v14, v15
	v_mov_b64_e32 v[14:15], s[24:25]
	v_mov_b64_e32 v[18:19], s[24:25]
	v_mov_b64_e32 v[16:17], s[26:27]
	v_mov_b64_e32 v[20:21], s[26:27]
	s_waitcnt lgkmcnt(8)
	s_nop 1
	v_mfma_f32_16x16x32_f16 v[42:45], v[76:79], v[100:103], v[42:45]
	v_mfma_f32_16x16x32_f16 v[38:41], v[72:75], v[100:103], v[38:41]
	v_mfma_f32_16x16x32_f16 v[14:17], v[68:71], v[100:103], v[14:17]
	v_mfma_f32_16x16x32_f16 v[18:21], v[64:67], v[100:103], v[18:21]
	v_mfma_f32_16x16x32_f16 v[22:25], v[60:63], v[100:103], v[22:25]
	v_mfma_f32_16x16x32_f16 v[26:29], v[88:91], v[100:103], v[26:29]
	v_mfma_f32_16x16x32_f16 v[30:33], v[92:95], v[100:103], v[30:33]
	v_mfma_f32_16x16x32_f16 v[34:37], v[96:99], v[100:103], v[34:37]
	v_lshlrev_b32_e32 v103, 4, v150
	s_waitcnt lgkmcnt(0)
	s_nop 1
	v_mfma_f32_16x16x32_f16 v[42:45], v[0:3], v[104:107], v[42:45]
	v_mfma_f32_16x16x32_f16 v[38:41], v[4:7], v[104:107], v[38:41]
	v_mfma_f32_16x16x32_f16 v[14:17], v[8:11], v[104:107], v[14:17]
	v_mfma_f32_16x16x32_f16 v[18:21], v[46:49], v[104:107], v[18:21]
	v_mfma_f32_16x16x32_f16 v[22:25], v[50:53], v[104:107], v[22:25]
	v_mfma_f32_16x16x32_f16 v[26:29], v[56:59], v[104:107], v[26:29]
	v_mfma_f32_16x16x32_f16 v[30:33], v[84:87], v[104:107], v[30:33]
	v_mfma_f32_16x16x32_f16 v[34:37], v[80:83], v[104:107], v[34:37]
	v_lshlrev_b32_e32 v0, 11, v193
	v_mov_b32_e32 v1, v201
	s_nop 15
	s_nop 7
	v_lshl_add_u64 v[0:1], v[210:211], 0, v[0:1]
	v_cndmask_b32_e64 v6, 0, v42, s[0:1]
	v_cndmask_b32_e64 v7, 0, v43, s[0:1]
	v_cndmask_b32_e64 v8, 0, v44, s[0:1]
	v_cndmask_b32_e64 v9, 0, v45, s[0:1]
	v_cndmask_b32_e64 v10, 0, v38, s[0:1]
	v_cndmask_b32_e64 v11, 0, v39, s[0:1]
	v_cndmask_b32_e64 v12, 0, v40, s[0:1]
	v_cndmask_b32_e64 v13, 0, v41, s[0:1]
	global_load_dwordx4 v[50:53], v[0:1], off offset:16
	global_load_dwordx4 v[46:49], v[0:1], off
	global_load_dwordx4 v[42:45], v[0:1], off offset:144
	global_load_dwordx4 v[38:41], v[0:1], off offset:128
	v_lshl_add_u32 v2, v220, 4, s14
	v_lshl_or_b32 v55, v207, 1, v2
	v_or_b32_e32 v2, s13, v220
	v_ashrrev_i32_e32 v3, 31, v2
	v_lshlrev_b32_e32 v0, 7, v109
	v_mov_b32_e32 v109, v201
	v_lshlrev_b64 v[2:3], 21, v[2:3]
	v_or3_b32 v104, v0, v103, s21
	v_lshl_add_u64 v[0:1], s[4:5], 0, v[108:109]
	s_cselect_b64 s[4:5], -1, 0
	v_lshl_add_u64 v[2:3], s[6:7], 0, v[2:3]
	s_ashr_i32 s3, s2, 31
	v_lshl_add_u64 v[2:3], s[2:3], 2, v[2:3]
	v_lshlrev_b32_e32 v4, 2, v208
	v_mov_b32_e32 v5, v201
	v_lshl_add_u64 v[96:97], v[2:3], 0, v[4:5]
	v_lshl_add_u32 v2, v214, 10, v54
	v_ashrrev_i32_e32 v3, 31, v2
	v_lshl_add_u64 v[2:3], v[2:3], 2, s[6:7]
	s_mov_b64 s[2:3], 0x8000000
	v_lshl_add_u64 v[98:99], v[2:3], 0, s[2:3]
	s_mov_b64 s[2:3], 0x8040000
	v_lshl_add_u64 v[100:101], v[2:3], 0, s[2:3]
	s_lshl_b32 s2, s19, 14
	s_lshl_b32 s3, s18, 9
	s_add_i32 s2, s2, s3
	v_mbcnt_lo_u32_b32 v2, -1, 0
	v_add_u32_e32 v106, s2, v55
	v_mbcnt_hi_u32_b32 v2, -1, v2
	v_mov_b64_e32 v[54:55], v[200:201]
	v_mov_b64_e32 v[58:59], v[200:201]
	v_cndmask_b32_e64 v14, 0, v14, s[0:1]
	v_cndmask_b32_e64 v15, 0, v15, s[0:1]
	v_cndmask_b32_e64 v16, 0, v16, s[0:1]
	v_cndmask_b32_e64 v17, 0, v17, s[0:1]
	v_cndmask_b32_e64 v18, 0, v18, s[0:1]
	v_cndmask_b32_e64 v19, 0, v19, s[0:1]
	v_cndmask_b32_e64 v20, 0, v20, s[0:1]
	v_cndmask_b32_e64 v21, 0, v21, s[0:1]
	v_cndmask_b32_e64 v22, 0, v22, s[0:1]
	v_cndmask_b32_e64 v23, 0, v23, s[0:1]
	v_cndmask_b32_e64 v24, 0, v24, s[0:1]
	v_cndmask_b32_e64 v25, 0, v25, s[0:1]
	v_cndmask_b32_e64 v26, 0, v26, s[0:1]
	v_cndmask_b32_e64 v27, 0, v27, s[0:1]
	v_cndmask_b32_e64 v28, 0, v28, s[0:1]
	v_cndmask_b32_e64 v29, 0, v29, s[0:1]
	v_cndmask_b32_e64 v30, 0, v30, s[0:1]
	v_cndmask_b32_e64 v31, 0, v31, s[0:1]
	v_cndmask_b32_e64 v32, 0, v32, s[0:1]
	v_cndmask_b32_e64 v33, 0, v33, s[0:1]
	v_cndmask_b32_e64 v34, 0, v34, s[0:1]
	v_cndmask_b32_e64 v35, 0, v35, s[0:1]
	v_cndmask_b32_e64 v36, 0, v36, s[0:1]
	v_cndmask_b32_e64 v37, 0, v37, s[0:1]
	v_lshlrev_b32_e32 v105, 9, v207
	s_mov_b64 s[6:7], 0
	s_mov_b32 s18, 0x40004000
	v_lshl_or_b32 v107, v2, 2, 32
	v_mov_b32_e32 v108, 0
	v_mov_b64_e32 v[56:57], v[202:203]
	v_mov_b64_e32 v[60:61], v[202:203]
	s_mov_b32 s24, 0
	v_lshl_add_u32 v166, s19, 14, v104
	v_mov_b32_e32 v177, 0
	s_mov_b32 s37, 0x4038aa3b
	s_mov_b32 s38, 0xbfb8aa3b
	v_lshlrev_b32_e32 v222, 4, v198
	ds_read_b128 v[130:133], v222
	ds_read_b128 v[126:129], v222 offset:1024
	ds_read_b128 v[122:125], v222 offset:2048
	ds_read_b128 v[118:121], v222 offset:3072
	ds_read_b128 v[114:117], v222 offset:4096
	ds_read_b128 v[110:113], v222 offset:5120
	ds_read_b128 v[194:197], v222 offset:6144
	ds_read_b128 v[202:205], v222 offset:7168
	ds_read_b128 v[162:165], v222 offset:8192
	ds_read_b128 v[158:161], v222 offset:9216
	ds_read_b128 v[154:157], v222 offset:10240
	ds_read_b128 v[150:153], v222 offset:11264
	ds_read_b128 v[146:149], v222 offset:12288
	ds_read_b128 v[142:145], v222 offset:13312
	ds_read_b128 v[138:141], v222 offset:14336
	ds_read_b128 v[134:137], v222 offset:15360
	s_waitcnt vmcnt(0)
	v_mul_f32_e32 v185, 0xbfb8aa3b, v185
	v_mul_f32_e32 v186, 0xbfb8aa3b, v186
	v_mul_f32_e32 v187, 0x4038aa3b, v187
	v_mul_f32_e32 v188, 0xbfb8aa3b, v188
	v_cvt_pk_f16_f32 v180, v46, v47
	v_cvt_pk_f16_f32 v181, v48, v49
	v_cvt_pk_f16_f32 v182, v50, v51
	v_cvt_pk_f16_f32 v183, v52, v53
	v_cvt_pk_f16_f32 v218, v38, v39
	v_cvt_pk_f16_f32 v219, v40, v41
	v_cvt_pk_f16_f32 v220, v42, v43
	v_cvt_pk_f16_f32 v221, v44, v45
	s_mov_b32 s25, 1
	v_bitop3_b32 v2, s25, v193, 1 bitop3:0x6c
	v_add_u32_e32 v2, s25, v2
	v_min_i32_e32 v2, 0x1ff, v2
	s_and_b32 s12, s25, 1
	v_lshlrev_b32_e32 v200, 11, v2
	v_lshl_add_u64 v[2:3], v[210:211], 0, v[200:201]
	s_lshl_b32 s14, s12, 8
	v_lshl_add_u64 v[4:5], v[2:3], 0, s[14:15]
	global_load_dwordx4 v[46:49], v[4:5], off
	global_load_dwordx4 v[50:53], v[4:5], off offset:16
	global_load_dwordx4 v[38:41], v[4:5], off offset:128
	global_load_dwordx4 v[42:45], v[4:5], off offset:144
.Lstep_top:
	s_and_b32 s16, s24, 1
	v_cmp_eq_u32_e64 s[2:3], s16, v193
	s_xor_b32 s33, s16, 1
	s_lshl_b32 s28, s33, 17
	s_add_i32 s25, s24, 1
	s_add_i32 s27, s24, 2
	s_mov_b32 s17, 0
	s_cmp_eq_u32 s24, 0
	s_cbranch_scc1 .Lpoll_issued
	buffer_load_dwordx4 v[62:65], v166, s[8:11], s28 offen sc1
	buffer_load_dwordx4 v[66:69], v166, s[8:11], s28 offen offset:512 sc1
	buffer_load_dwordx4 v[70:73], v166, s[8:11], s28 offen offset:1024 sc1
	buffer_load_dwordx4 v[74:77], v166, s[8:11], s28 offen offset:1536 sc1
	buffer_load_dwordx4 v[78:81], v166, s[8:11], s28 offen offset:2048 sc1
	buffer_load_dwordx4 v[82:85], v166, s[8:11], s28 offen offset:2560 sc1
	buffer_load_dwordx4 v[86:89], v166, s[8:11], s28 offen offset:3072 sc1
	buffer_load_dwordx4 v[90:93], v166, s[8:11], s28 offen offset:3584 sc1
.Lpoll_issued:
	s_andn2_b64 exec, exec, s[2:3]
	v_mov_b64_e32 v[6:7], 0
	v_mov_b64_e32 v[8:9], 0
	v_mov_b64_e32 v[10:11], 0
	v_mov_b64_e32 v[12:13], 0
	v_mov_b64_e32 v[14:15], 0
	v_mov_b64_e32 v[16:17], 0
	v_mov_b64_e32 v[18:19], 0
	v_mov_b64_e32 v[20:21], 0
	v_mov_b64_e32 v[22:23], 0
	v_mov_b64_e32 v[24:25], 0
	v_mov_b64_e32 v[26:27], 0
	v_mov_b64_e32 v[28:29], 0
	v_mov_b64_e32 v[30:31], 0
	v_mov_b64_e32 v[32:33], 0
	v_mov_b64_e32 v[34:35], 0
	v_mov_b64_e32 v[36:37], 0
	s_mov_b64 exec, -1
	s_waitcnt lgkmcnt(0)
	v_mfma_f32_16x16x32_f16 v[6:9], v[130:133], v[180:183], v[6:9]
	s_add_i32 s12, s24, -1
	s_bfe_i32 s13, s12, 0x10001
	s_and_b32 s30, s13, 0x40004000
	v_mfma_f32_16x16x32_f16 v[10:13], v[126:129], v[180:183], v[10:13]
	v_mov_b32_e32 v3, 0xbfffbfff
	v_cndmask_b32_e64 v167, 0, v3, s[2:3]
	s_lshl_b32 s34, s24, 13
	v_mfma_f32_16x16x32_f16 v[14:17], v[122:125], v[180:183], v[14:17]
	s_and_b32 s34, s34, 0x4000
	s_lshl_b32 s14, s24, 10
	v_lshl_add_u64 v[178:179], s[14:15], 2, v[96:97]
	v_mfma_f32_16x16x32_f16 v[18:21], v[118:121], v[180:183], v[18:21]
	v_bitop3_b32 v2, s27, v193, 1 bitop3:0x6c
	v_add_u32_e32 v2, s27, v2
	v_min_i32_e32 v2, 0x1ff, v2
	v_mfma_f32_16x16x32_f16 v[22:25], v[114:117], v[180:183], v[22:25]
	s_and_b32 s12, s27, 1
	v_lshlrev_b32_e32 v200, 11, v2
	v_lshl_add_u64 v[2:3], v[210:211], 0, v[200:201]
	v_mfma_f32_16x16x32_f16 v[26:29], v[110:113], v[180:183], v[26:29]
	s_lshl_b32 s14, s12, 8
	v_lshl_add_u64 v[4:5], v[2:3], 0, s[14:15]
	s_lshl_b32 s35, s16, 14
	v_mfma_f32_16x16x32_f16 v[30:33], v[194:197], v[180:183], v[30:33]
	s_bitset1_b32 s35, 17
	s_add_i32 s26, s35, s21
	v_lshlrev_b32_e32 v2, 4, v217
	v_mfma_f32_16x16x32_f16 v[34:37], v[202:205], v[180:183], v[34:37]
	v_add3_u32 v174, s26, v2, v103
	s_lshl_b32 s12, s20, 4
	s_add_i32 s12, s12, s35
	s_waitcnt lgkmcnt(0)
	v_mfma_f32_16x16x32_f16 v[6:9], v[162:165], v[218:221], v[6:9]
	v_add3_u32 v175, s12, v105, v103
	v_lshl_add_u32 v176, s16, 17, v106
	v_mfma_f32_16x16x32_f16 v[10:13], v[158:161], v[218:221], v[10:13]
	s_and_b32 s31, s24, 15
	s_and_b32 s12, s24, 0x1f0
	v_mfma_f32_16x16x32_f16 v[14:17], v[154:157], v[218:221], v[14:17]
	s_add_i32 s12, s23, s12
	s_min_i32 s12, s12, 0x1ff
	s_waitcnt vmcnt(7)
	v_mfma_f32_16x16x32_f16 v[18:21], v[150:153], v[218:221], v[18:21]
	v_bitop3_b32 v168, v62, v63, s30 bitop3:0x7e
	v_bitop3_b32 v169, v64, v65, s30 bitop3:0x7e
	v_mfma_f32_16x16x32_f16 v[22:25], v[146:149], v[218:221], v[22:25]
	v_bitop3_b32 v168, v168, v169, s18 bitop3:0xa8
	v_cmp_ne_u32_e32 vcc, 0, v168
	v_mfma_f32_16x16x32_f16 v[26:29], v[142:145], v[218:221], v[26:29]
	v_and_b32_e32 v62, v62, v167
	v_and_b32_e32 v63, v63, v167
	v_mfma_f32_16x16x32_f16 v[30:33], v[138:141], v[218:221], v[30:33]
	v_and_b32_e32 v64, v64, v167
	v_and_b32_e32 v65, v65, v167
	v_mfma_f32_16x16x32_f16 v[34:37], v[134:137], v[218:221], v[34:37]
	s_ashr_i32 s13, s12, 31
	s_lshl_b64 s[12:13], s[12:13], 11
	v_lshl_add_u64 v[172:173], v[0:1], 0, s[12:13]
	s_cmp_eq_u32 s24, 0
	s_cbranch_scc1 .Lfirst_step
	s_cbranch_vccnz .Lrestart0

.Lfast1:
	v_mfma_f32_16x16x32_f16 v[6:9], a[4:7], v[66:69], v[6:9]
	v_xor_b32_e32 v222, 0x4000, v222
	ds_read_b128 v[130:133], v222
	v_mfma_f32_16x16x32_f16 v[10:13], a[36:39], v[66:69], v[10:13]
	ds_read_b128 v[126:129], v222 offset:1024
	ds_read_b128 v[122:125], v222 offset:2048
	v_mfma_f32_16x16x32_f16 v[14:17], a[68:71], v[66:69], v[14:17]
	s_waitcnt vmcnt(5)
	v_mfma_f32_16x16x32_f16 v[18:21], a[100:103], v[66:69], v[18:21]
	v_bitop3_b32 v168, v70, v71, s30 bitop3:0x7e
	v_bitop3_b32 v169, v72, v73, s30 bitop3:0x7e
	v_mfma_f32_16x16x32_f16 v[22:25], a[132:135], v[66:69], v[22:25]
	v_bitop3_b32 v168, v168, v169, s18 bitop3:0xa8
	v_cmp_ne_u32_e32 vcc, 0, v168
	v_mfma_f32_16x16x32_f16 v[26:29], a[164:167], v[66:69], v[26:29]
	v_and_b32_e32 v70, v70, v167
	v_and_b32_e32 v71, v71, v167
	v_mfma_f32_16x16x32_f16 v[30:33], a[196:199], v[66:69], v[30:33]
	v_and_b32_e32 v72, v72, v167
	v_and_b32_e32 v73, v73, v167
	v_mfma_f32_16x16x32_f16 v[34:37], a[228:231], v[66:69], v[34:37]
	s_cbranch_vccnz .Lrestart2
.Lfast2:
	v_mfma_f32_16x16x32_f16 v[6:9], a[8:11], v[70:73], v[6:9]
	ds_read_b128 v[118:121], v222 offset:3072
	ds_read_b128 v[114:117], v222 offset:4096
	v_mfma_f32_16x16x32_f16 v[10:13], a[40:43], v[70:73], v[10:13]
	ds_read_b128 v[110:113], v222 offset:5120
	ds_read_b128 v[194:197], v222 offset:6144
	v_mfma_f32_16x16x32_f16 v[14:17], a[72:75], v[70:73], v[14:17]
	s_waitcnt vmcnt(4)
	v_mfma_f32_16x16x32_f16 v[18:21], a[104:107], v[70:73], v[18:21]
	v_bitop3_b32 v168, v74, v75, s30 bitop3:0x7e
	v_bitop3_b32 v169, v76, v77, s30 bitop3:0x7e
	v_mfma_f32_16x16x32_f16 v[22:25], a[136:139], v[70:73], v[22:25]
	v_bitop3_b32 v168, v168, v169, s18 bitop3:0xa8
	v_cmp_ne_u32_e32 vcc, 0, v168
	v_mfma_f32_16x16x32_f16 v[26:29], a[168:171], v[70:73], v[26:29]
	v_and_b32_e32 v74, v74, v167
	v_and_b32_e32 v75, v75, v167
	v_mfma_f32_16x16x32_f16 v[30:33], a[200:203], v[70:73], v[30:33]
	v_and_b32_e32 v76, v76, v167
	v_and_b32_e32 v77, v77, v167
	v_mfma_f32_16x16x32_f16 v[34:37], a[232:235], v[70:73], v[34:37]
	s_cbranch_vccnz .Lrestart3
.Lfast3:
	v_mfma_f32_16x16x32_f16 v[6:9], a[12:15], v[74:77], v[6:9]
	ds_read_b128 v[202:205], v222 offset:7168
	ds_read_b128 v[162:165], v222 offset:8192
	v_mfma_f32_16x16x32_f16 v[10:13], a[44:47], v[74:77], v[10:13]
	ds_read_b128 v[158:161], v222 offset:9216
	ds_read_b128 v[154:157], v222 offset:10240
	v_mfma_f32_16x16x32_f16 v[14:17], a[76:79], v[74:77], v[14:17]
	s_waitcnt vmcnt(3)
	v_mfma_f32_16x16x32_f16 v[18:21], a[108:111], v[74:77], v[18:21]
	v_bitop3_b32 v168, v78, v79, s30 bitop3:0x7e
	v_bitop3_b32 v169, v80, v81, s30 bitop3:0x7e
	v_mfma_f32_16x16x32_f16 v[22:25], a[140:143], v[74:77], v[22:25]
	v_bitop3_b32 v168, v168, v169, s18 bitop3:0xa8
	v_cmp_ne_u32_e32 vcc, 0, v168
	v_mfma_f32_16x16x32_f16 v[26:29], a[172:175], v[74:77], v[26:29]
	v_and_b32_e32 v78, v78, v167
	v_and_b32_e32 v79, v79, v167
	v_mfma_f32_16x16x32_f16 v[30:33], a[204:207], v[74:77], v[30:33]
	v_and_b32_e32 v80, v80, v167
	v_and_b32_e32 v81, v81, v167
	v_mfma_f32_16x16x32_f16 v[34:37], a[236:239], v[74:77], v[34:37]
	s_cbranch_vccnz .Lrestart4
.Lfast4:
	v_mfma_f32_16x16x32_f16 v[6:9], a[16:19], v[78:81], v[6:9]
	ds_read_b128 v[150:153], v222 offset:11264
	ds_read_b128 v[146:149], v222 offset:12288
	v_mfma_f32_16x16x32_f16 v[10:13], a[48:51], v[78:81], v[10:13]
	ds_read_b128 v[142:145], v222 offset:13312
	ds_read_b128 v[138:141], v222 offset:14336
	v_mfma_f32_16x16x32_f16 v[14:17], a[80:83], v[78:81], v[14:17]
	s_waitcnt vmcnt(2)
	v_mfma_f32_16x16x32_f16 v[18:21], a[112:115], v[78:81], v[18:21]
	v_bitop3_b32 v168, v82, v83, s30 bitop3:0x7e
	v_bitop3_b32 v169, v84, v85, s30 bitop3:0x7e
	v_mfma_f32_16x16x32_f16 v[22:25], a[144:147], v[78:81], v[22:25]
	v_bitop3_b32 v168, v168, v169, s18 bitop3:0xa8
	v_cmp_ne_u32_e32 vcc, 0, v168
	v_mfma_f32_16x16x32_f16 v[26:29], a[176:179], v[78:81], v[26:29]
	v_and_b32_e32 v82, v82, v167
	v_and_b32_e32 v83, v83, v167
	v_mfma_f32_16x16x32_f16 v[30:33], a[208:211], v[78:81], v[30:33]
	v_and_b32_e32 v84, v84, v167
	v_and_b32_e32 v85, v85, v167
	v_mfma_f32_16x16x32_f16 v[34:37], a[240:243], v[78:81], v[34:37]
	s_cbranch_vccnz .Lrestart5
.Lfast5:
	v_mfma_f32_16x16x32_f16 v[6:9], a[20:23], v[82:85], v[6:9]
	ds_read_b128 v[134:137], v222 offset:15360
	v_mfma_f32_16x16x32_f16 v[10:13], a[52:55], v[82:85], v[10:13]
	v_mfma_f32_16x16x32_f16 v[14:17], a[84:87], v[82:85], v[14:17]
	s_waitcnt vmcnt(1)
	v_mfma_f32_16x16x32_f16 v[18:21], a[116:119], v[82:85], v[18:21]
	v_bitop3_b32 v168, v86, v87, s30 bitop3:0x7e
	v_bitop3_b32 v169, v88, v89, s30 bitop3:0x7e
	v_mfma_f32_16x16x32_f16 v[22:25], a[148:151], v[82:85], v[22:25]
	v_bitop3_b32 v168, v168, v169, s18 bitop3:0xa8
	v_cmp_ne_u32_e32 vcc, 0, v168
	v_mfma_f32_16x16x32_f16 v[26:29], a[180:183], v[82:85], v[26:29]
	v_and_b32_e32 v86, v86, v167
	v_and_b32_e32 v87, v87, v167
	v_mfma_f32_16x16x32_f16 v[30:33], a[212:215], v[82:85], v[30:33]
	v_and_b32_e32 v88, v88, v167
	v_and_b32_e32 v89, v89, v167
	v_mfma_f32_16x16x32_f16 v[34:37], a[244:247], v[82:85], v[34:37]
	s_cbranch_vccnz .Lrestart6

.Lno_warm:
	s_waitcnt lgkmcnt(0)
	s_barrier
	ds_read_b128 v[2:5], v175
	ds_read_b128 v[224:227], v175 offset:4096
	ds_read_b128 v[228:231], v175 offset:8192
	ds_read_b128 v[232:235], v175 offset:12288
	s_waitcnt lgkmcnt(0)
	v_pk_add_f32 v[4:5], v[4:5], v[226:227]
	v_pk_add_f32 v[2:3], v[2:3], v[224:225]
	v_pk_add_f32 v[4:5], v[4:5], v[230:231]
	v_pk_add_f32 v[2:3], v[2:3], v[228:229]
	v_pk_add_f32 v[4:5], v[4:5], v[234:235]
	v_pk_add_f32 v[2:3], v[2:3], v[232:233]
	v_fma_f32 v4, v4, s37, v187
	v_fma_f32 v2, v2, s38, v185
	v_exp_f32_e32 v4, v4
	v_fma_f32 v3, v3, s38, v186
	v_exp_f32_e32 v2, v2
	v_fma_f32 v5, v5, s38, v188
	v_exp_f32_e32 v3, v3
	v_add_f32_e32 v4, 1.0, v4
	v_add_f32_e32 v2, 1.0, v2
	v_rcp_f32_e32 v4, v4
	v_rcp_f32_e32 v2, v2
	v_add_f32_e32 v3, 1.0, v3
	v_rcp_f32_e32 v3, v3
	v_exp_f32_e32 v5, v5
	v_fma_f32 v4, v4, -2.0, 1.0
	v_mul_f32_e32 v2, v2, v4
	v_add_f32_e32 v4, 1.0, v5
	v_fmac_f32_e32 v2, v177, v3
	v_rcp_f32_e32 v5, v4
	v_mul_f32_e32 v3, 0x4038aa3b, v2
	v_exp_f32_e32 v3, v3
	v_mov_b32_e32 v177, v2
	v_add_f32_e32 v3, 1.0, v3
	v_rcp_f32_e32 v3, v3
	s_nop 0
	v_fma_f32 v3, v3, -2.0, 1.0
	v_mul_f32_e32 v4, v5, v3
	v_fma_mixlo_f16 v3, v5, v3, 0
	v_and_b32_e32 v3, 0xffffbfff, v3
	v_or_b32_sdwa v108, s34, v3 dst_sel:DWORD dst_unused:UNUSED_PAD src0_sel:DWORD src1_sel:WORD_0
	s_nop 1
	v_mov_b32_dpp v109, v108 row_ror:8 row_mask:0xf bank_mask:0xf
	v_mov_b32_dpp v5, v4 row_ror:8 row_mask:0xf bank_mask:0xf
	s_and_saveexec_b64 s[12:13], s[0:1]
	v_lshl_or_b32 v108, v109, 16, v108
	s_andn2_b64 vcc, exec, s[4:5]
	s_cbranch_vccnz .Lpub_sc1
	buffer_store_dword v108, v176, s[8:11], 0 offen

.Lfirst_step:
	s_waitcnt vmcnt(0)
	v_cvt_pk_f16_f32 v180, v46, v47
	v_cvt_pk_f16_f32 v181, v48, v49
	v_cvt_pk_f16_f32 v182, v50, v51
	v_cvt_pk_f16_f32 v183, v52, v53
	v_cvt_pk_f16_f32 v218, v38, v39
	v_cvt_pk_f16_f32 v219, v40, v41
	v_cvt_pk_f16_f32 v220, v42, v43
	v_cvt_pk_f16_f32 v221, v44, v45
	v_xor_b32_e32 v222, 0x4000, v222
	ds_read_b128 v[130:133], v222
	ds_read_b128 v[126:129], v222 offset:1024
	ds_read_b128 v[122:125], v222 offset:2048
	ds_read_b128 v[118:121], v222 offset:3072
	ds_read_b128 v[114:117], v222 offset:4096
	ds_read_b128 v[110:113], v222 offset:5120
	ds_read_b128 v[194:197], v222 offset:6144
	ds_read_b128 v[202:205], v222 offset:7168
	ds_read_b128 v[162:165], v222 offset:8192
	ds_read_b128 v[158:161], v222 offset:9216
	ds_read_b128 v[154:157], v222 offset:10240
	ds_read_b128 v[150:153], v222 offset:11264
	ds_read_b128 v[146:149], v222 offset:12288
	ds_read_b128 v[142:145], v222 offset:13312
	ds_read_b128 v[138:141], v222 offset:14336
	ds_read_b128 v[134:137], v222 offset:15360
	s_branch .Lall_chunks_done
